# baseline (speedup 1.0000x reference)
_Z6conv_kILi128ELi256ELi3ELi64ELi1ELi1ELb0EEvPKDF16_S1_PKfS3_PDF16_S4_S1_fS3_S3_S3_S3_:
	s_lshl_b32 s3, s2, 3
	s_load_dwordx2 s[20:21], s[0:1], 0x0
	s_load_dwordx2 s[84:85], s[0:1], 0x8
	s_load_dwordx4 s[4:7], s[0:1], 0x10
	s_load_dwordx2 s[18:19], s[0:1], 0x30
	s_and_b32 s3, s3, 56
	s_ashr_i32 s8, s2, 5
	s_add_i32 s3, s3, s8
	v_readfirstlane_b32 s27, v0
	s_lshl_b32 s8, s3, 2
	s_bfe_u32 s22, s2, 0x20003
	s_and_b32 s24, s8, 56
	s_lshr_b32 s33, s27, 6
	s_ashr_i32 s25, s3, 4
	s_and_b32 s15, s2, 32
	s_lshl_b32 s2, s22, 8
	v_bfe_u32 v24, v0, 3, 3
	v_and_b32_e32 v2, 7, v0
	s_waitcnt lgkmcnt(0)
	s_add_u32 s2, s4, s2
	v_bitop3_b32 v2, v24, v2, 6 bitop3:0x6c
	s_addc_u32 s3, s5, 0
	v_and_b32_e32 v18, 48, v0
	v_mov_b32_e32 v19, 0
	v_lshlrev_b32_e32 v20, 3, v2
	v_lshl_add_u64 v[2:3], s[2:3], 0, v[18:19]
	s_load_dword s14, s[6:7], 0x0
	global_load_dwordx4 v[14:17], v[2:3], off
	v_lshl_add_u64 v[4:5], v[2:3], 0, 64
	s_mov_b64 s[2:3], 0x80
	global_load_dwordx4 v[10:13], v[4:5], off
	v_lshl_add_u64 v[4:5], v[2:3], 0, s[2:3]
	s_mov_b64 s[2:3], 0xc0
	v_lshl_add_u64 v[2:3], v[2:3], 0, s[2:3]
	v_lshl_or_b32 v18, s33, 3, v24
	s_mov_b32 s2, 0x1e1e1e1f
	v_mul_hi_u32 v21, v18, s2
	v_lshrrev_b32_e32 v21, 2, v21
	s_movk_i32 s4, 0xffde
	s_add_i32 s12, s24, -1
	global_load_dwordx4 v[6:9], v[4:5], off
	v_mul_lo_u32 v22, v21, s4
	v_add_u32_e32 v46, s12, v21
	s_add_i32 s13, s15, -1
	s_movk_i32 s5, 0x154
	global_load_dwordx4 v[2:5], v[2:3], off
	v_add3_u32 v47, s13, v18, v22
	v_cmp_gt_u32_e32 vcc, s5, v18
	v_cmp_gt_u32_e64 s[2:3], 64, v46
	s_and_b64 s[2:3], vcc, s[2:3]
	v_cmp_gt_u32_e32 vcc, 64, v47
	v_and_b32_e32 v1, 63, v0
	s_and_b64 vcc, s[2:3], vcc
	v_mov_b64_e32 v[22:23], s[18:19]
	v_lshlrev_b32_e32 v18, 1, v20
	s_and_saveexec_b64 s[2:3], vcc
	s_lshl_b32 s6, s25, 13
	v_lshlrev_b32_e32 v21, 6, v46
	v_or3_b32 v22, v21, s6, v47
	v_ashrrev_i32_e32 v23, 31, v22
	v_lshlrev_b64 v[22:23], 7, v[22:23]
	v_lshl_add_u64 v[22:23], s[20:21], 0, v[22:23]
	v_lshl_add_u64 v[22:23], v[22:23], 0, v[18:19]
	s_or_b64 exec, exec, s[2:3]
	s_lshl_b32 s36, s33, 10
	v_lshlrev_b32_e32 v21, 4, v1
	v_or_b32_e32 v19, s36, v21
	s_add_i32 s7, s33, 8
	v_readfirstlane_b32 s2, v19
	s_mov_b32 m0, s2
	v_lshl_or_b32 v19, s7, 3, v24
	global_load_lds_dwordx4 v[22:23], off
	s_mov_b32 s6, 0x3c3c3c3d
	v_mul_hi_u32 v22, v19, s6
	v_lshrrev_b32_e32 v22, 3, v22
	v_mul_lo_u32 v23, v22, s4
	v_add_u32_e32 v48, s12, v22
	v_add3_u32 v49, s13, v19, v23
	v_cmp_gt_u32_e64 s[2:3], s5, v19
	v_cmp_gt_u32_e64 s[4:5], 64, v48
	s_and_b64 s[4:5], s[2:3], s[4:5]
	v_cmp_gt_u32_e64 s[2:3], 64, v49
	s_and_b64 s[2:3], s[4:5], s[2:3]
	v_mov_b64_e32 v[22:23], s[18:19]
	s_and_saveexec_b64 s[4:5], s[2:3]
	s_lshl_b32 s8, s25, 13
	v_lshlrev_b32_e32 v19, 6, v48
	v_or3_b32 v22, v19, s8, v49
	v_ashrrev_i32_e32 v23, 31, v22
	v_lshlrev_b64 v[22:23], 7, v[22:23]
	v_lshl_add_u64 v[22:23], s[20:21], 0, v[22:23]
	v_mov_b32_e32 v19, 0
	v_lshl_add_u64 v[22:23], v[22:23], 0, v[18:19]
	s_or_b64 exec, exec, s[4:5]
	s_lshl_b32 s37, s7, 10
	v_or_b32_e32 v19, s37, v21
	s_add_i32 s10, s33, 16
	v_readfirstlane_b32 s4, v19
	s_mov_b32 m0, s4
	v_lshl_or_b32 v19, s10, 3, v24
	global_load_lds_dwordx4 v[22:23], off
	v_mul_hi_u32 v22, v19, s6
	v_lshrrev_b32_e32 v22, 3, v22
	s_movk_i32 s8, 0xffde
	v_mul_lo_u32 v23, v22, s8
	v_add_u32_e32 v58, s12, v22
	s_movk_i32 s9, 0x154
	v_add3_u32 v59, s13, v19, v23
	v_cmp_gt_u32_e64 s[4:5], s9, v19
	v_cmp_gt_u32_e64 s[6:7], 64, v58
	s_and_b64 s[6:7], s[4:5], s[6:7]
	v_cmp_gt_u32_e64 s[4:5], 64, v59
	s_and_b64 s[4:5], s[6:7], s[4:5]
	v_mov_b64_e32 v[22:23], s[18:19]
	s_and_saveexec_b64 s[6:7], s[4:5]
	s_lshl_b32 s11, s25, 13
	v_lshlrev_b32_e32 v19, 6, v58
	v_or3_b32 v22, v19, s11, v59
	v_ashrrev_i32_e32 v23, 31, v22
	v_lshlrev_b64 v[22:23], 7, v[22:23]
	v_lshl_add_u64 v[22:23], s[20:21], 0, v[22:23]
	v_mov_b32_e32 v19, 0
	v_lshl_add_u64 v[22:23], v[22:23], 0, v[18:19]
	s_or_b64 exec, exec, s[6:7]
	s_lshl_b32 s38, s10, 10
	v_or_b32_e32 v19, s38, v21
	s_add_i32 s11, s33, 24
	v_readfirstlane_b32 s6, v19
	s_mov_b32 m0, s6
	v_lshl_or_b32 v19, s11, 3, v24
	global_load_lds_dwordx4 v[22:23], off
	s_mov_b32 s10, 0x3c3c3c3d
	v_mul_hi_u32 v22, v19, s10
	v_lshrrev_b32_e32 v22, 3, v22
	v_mul_lo_u32 v23, v22, s8
	v_add_u32_e32 v60, s12, v22
	v_add3_u32 v61, s13, v19, v23
	v_cmp_gt_u32_e64 s[6:7], s9, v19
	v_cmp_gt_u32_e64 s[8:9], 64, v60
	s_and_b64 s[8:9], s[6:7], s[8:9]
	v_cmp_gt_u32_e64 s[6:7], 64, v61
	s_and_b64 s[6:7], s[8:9], s[6:7]
	v_mov_b64_e32 v[22:23], s[18:19]
	s_and_saveexec_b64 s[8:9], s[6:7]
	s_lshl_b32 s16, s25, 13
	v_lshlrev_b32_e32 v19, 6, v60
	v_or3_b32 v22, v19, s16, v61
	v_ashrrev_i32_e32 v23, 31, v22
	v_lshlrev_b64 v[22:23], 7, v[22:23]
	v_lshl_add_u64 v[22:23], s[20:21], 0, v[22:23]
	v_mov_b32_e32 v19, 0
	v_lshl_add_u64 v[22:23], v[22:23], 0, v[18:19]
	s_or_b64 exec, exec, s[8:9]
	s_lshl_b32 s39, s11, 10
	v_or_b32_e32 v19, s39, v21
	s_add_i32 s16, s33, 32
	v_readfirstlane_b32 s8, v19
	s_mov_b32 m0, s8
	v_lshl_or_b32 v19, s16, 3, v24
	global_load_lds_dwordx4 v[22:23], off
	v_mul_hi_u32 v22, v19, s10
	v_lshrrev_b32_e32 v22, 3, v22
	s_movk_i32 s8, 0xffde
	v_mul_lo_u32 v23, v22, s8
	v_add_u32_e32 v62, s12, v22
	s_movk_i32 s8, 0x154
	v_add3_u32 v63, s13, v19, v23
	v_cmp_gt_u32_e64 s[8:9], s8, v19
	v_cmp_gt_u32_e64 s[10:11], 64, v62
	s_and_b64 s[10:11], s[8:9], s[10:11]
	v_cmp_gt_u32_e64 s[8:9], 64, v63
	s_and_b64 s[8:9], s[10:11], s[8:9]
	s_xor_b64 s[10:11], s[8:9], -1
	s_and_saveexec_b64 s[28:29], s[10:11]
	s_xor_b64 s[10:11], exec, s[28:29]
	s_lshl_b32 s17, s25, 13
	s_or_saveexec_b64 s[10:11], s[10:11]
	v_mov_b32_e32 v64, s17
	v_mov_b64_e32 v[22:23], s[18:19]
	s_xor_b64 exec, exec, s[10:11]
	s_lshl_b32 s17, s25, 13
	v_lshlrev_b32_e32 v19, 6, v62
	v_or3_b32 v22, v19, s17, v63
	v_ashrrev_i32_e32 v23, 31, v22
	v_lshlrev_b64 v[22:23], 7, v[22:23]
	v_lshl_add_u64 v[22:23], s[20:21], 0, v[22:23]
	v_mov_b32_e32 v19, 0
	v_lshl_add_u64 v[22:23], v[22:23], 0, v[18:19]
	v_mov_b32_e32 v64, s17
	s_or_b64 exec, exec, s[10:11]
	s_lshl_b32 s40, s16, 10
	v_or_b32_e32 v18, s40, v21
	s_add_i32 s23, s33, 40
	v_readfirstlane_b32 s10, v18
	s_mov_b32 m0, s10
	v_lshl_or_b32 v19, s23, 3, v24
	global_load_lds_dwordx4 v[22:23], off
	s_mov_b32 s10, 0x3c3c3c3d
	v_mul_hi_u32 v18, v19, s10
	v_lshrrev_b32_e32 v18, 3, v18
	s_movk_i32 s10, 0xffde
	s_mov_b64 s[16:17], s[84:85]
	v_mul_lo_u32 v22, v18, s10
	v_add_u32_e32 v18, s12, v18
	s_movk_i32 s10, 0x154
	v_add3_u32 v65, s13, v19, v22
	v_cmp_gt_u32_e64 s[10:11], s10, v19
	v_cmp_gt_u32_e64 s[12:13], 64, v18
	s_and_b64 s[12:13], s[10:11], s[12:13]
	v_cmp_gt_u32_e64 s[10:11], 64, v65
	s_and_b64 s[10:11], s[12:13], s[10:11]
	s_xor_b64 s[12:13], s[10:11], -1
	v_lshlrev_b32_e32 v66, 6, v18
	s_and_saveexec_b64 s[28:29], s[12:13]
	s_xor_b64 s[12:13], exec, s[28:29]
	v_lshlrev_b32_e32 v66, 6, v18
	s_or_saveexec_b64 s[12:13], s[12:13]
	v_mov_b64_e32 v[18:19], s[18:19]
	s_xor_b64 exec, exec, s[12:13]
	v_or3_b32 v18, v66, v64, v65
	v_ashrrev_i32_e32 v19, 31, v18
	v_lshlrev_b64 v[18:19], 7, v[18:19]
	v_lshl_add_u64 v[18:19], s[20:21], 0, v[18:19]
	v_lshlrev_b32_e32 v22, 1, v20
	v_mov_b32_e32 v23, 0
	v_lshl_add_u64 v[18:19], v[18:19], 0, v[22:23]
	s_or_b64 exec, exec, s[12:13]
	v_lshrrev_b32_e32 v129, 4, v1
	v_bitop3_b32 v23, v129, v0, 6 bitop3:0x78
	v_and_b32_e32 v128, 15, v0
	v_lshlrev_b32_e32 v23, 4, v23
	s_lshr_b32 s29, s27, 8
	v_lshl_or_b32 v23, v128, 7, v23
	v_lshl_or_b32 v23, s29, 13, v23
	s_lshl_b32 s41, s23, 10
	s_lshl_b32 s26, s22, 6
	s_and_b32 s28, s33, 3
	v_add_u32_e32 v132, 0x18000, v23
	v_or_b32_e32 v23, s41, v21
	s_lshl_b32 s22, s22, 13
	v_readfirstlane_b32 s23, v23
	s_waitcnt lgkmcnt(0)
	s_add_u32 s22, s16, s22
	s_mul_hi_u32 s44, s27, 0x38e38e39
	s_mov_b32 m0, s23
	s_addc_u32 s23, s17, 0
	s_lshr_b32 s16, s44, 10
	s_mul_i32 s16, s16, -9
	s_add_i32 s16, s16, s29
	s_lshl_b32 s34, s33, 11
	s_ashr_i32 s17, s16, 31
	s_add_i32 s33, s34, 0x18000
	s_lshl_b64 s[16:17], s[16:17], 15
	s_add_u32 s16, s22, s16
	s_addc_u32 s17, s23, s17
	s_add_i32 s42, s29, 2
	s_mul_hi_u32 s43, s42, 0xe38e38f
	v_lshl_or_b32 v22, v24, 6, s36
	s_movk_i32 s31, 0xdc0
	s_mul_i32 s43, s43, -9
	v_and_or_b32 v22, v22, s31, v20
	s_add_i32 s42, s43, s42
	global_load_lds_dwordx4 v[18:19], off
	v_lshlrev_b32_e32 v18, 1, v22
	v_mov_b32_e32 v19, 0
	s_mov_b32 m0, s33
	s_ashr_i32 s43, s42, 31
	v_lshl_add_u64 v[22:23], s[16:17], 0, v[18:19]
	global_load_lds_dwordx4 v18, s[16:17]
	s_mov_b64 s[16:17], 0x400
	s_add_i32 m0, s34, 0x18400
	s_lshl_b64 s[42:43], s[42:43], 15
	v_lshl_add_u64 v[22:23], v[22:23], 0, s[16:17]
	s_add_u32 s42, s22, s42
	global_load_lds_dwordx4 v[22:23], off
	s_addc_u32 s43, s23, s43
	s_add_i32 m0, s34, 0x1c000
	v_lshl_add_u64 v[22:23], s[42:43], 0, v[18:19]
	global_load_lds_dwordx4 v18, s[42:43]
	s_add_i32 s42, s29, 4
	s_mul_hi_u32 s43, s42, 0xe38e38f
	s_mul_i32 s43, s43, -9
	s_add_i32 s42, s43, s42
	s_ashr_i32 s43, s42, 31
	s_add_i32 m0, s34, 0x1c400
	s_lshl_b64 s[42:43], s[42:43], 15
	s_add_u32 s42, s22, s42
	v_lshl_add_u64 v[22:23], v[22:23], 0, s[16:17]
	s_addc_u32 s43, s23, s43
	global_load_lds_dwordx4 v[22:23], off
	s_add_i32 m0, s34, 0x20000
	v_lshl_add_u64 v[22:23], s[42:43], 0, v[18:19]
	global_load_lds_dwordx4 v18, s[42:43]
	v_lshl_add_u64 v[22:23], v[22:23], 0, s[16:17]
	s_add_i32 m0, s34, 0x20400
	s_lshr_b32 s34, s44, 9
	global_load_lds_dwordx4 v[22:23], off
	s_mul_i32 s34, s34, -9
	s_add_i32 s34, s34, s29
	s_mul_hi_i32 s42, s34, 0x55555556
	s_lshr_b32 s43, s42, 31
	s_mul_i32 s31, s28, 0x44
	s_add_i32 s42, s42, s43
	v_add_u32_e32 v130, s31, v128
	s_mul_i32 s42, s42, 31
	v_add_u32_e32 v131, 34, v130
	s_add_i32 s42, s42, s34
	s_bitcmp1_b32 s44, 9
	v_add_u32_e32 v30, s42, v130
	v_add_u32_e32 v38, s42, v131
	s_movk_i32 s42, 0x1000
	v_lshlrev_b32_e32 v68, 1, v20
	v_lshl_add_u32 v20, v48, 6, v64
	s_waitcnt vmcnt(4) lgkmcnt(0)
	s_barrier
	s_cselect_b32 s43, 0xc000, 0
	ds_read_b128 v[26:29], v132
	v_add3_u32 v48, v20, v49, s42
	v_lshl_add_u32 v20, v58, 6, v64
	ds_read_b128 v[22:25], v132 offset:2048
	v_bitop3_b32 v31, v30, v129, 6 bitop3:0x6c
	v_lshl_add_u32 v30, v30, 7, s43
	v_add3_u32 v58, v20, v59, s42
	v_lshl_add_u32 v20, v60, 6, v64
	v_lshl_or_b32 v134, v31, 4, v30
	ds_read_b128 v[34:37], v134
	v_lshl_add_u32 v46, v46, 6, v64
	v_add3_u32 v60, v20, v61, s42
	v_lshl_add_u32 v20, v62, 6, v64
	ds_read_b128 v[30:33], v134 offset:2048
	v_bitop3_b32 v39, v38, v129, 6 bitop3:0x6c
	v_lshl_add_u32 v38, v38, 7, s43
	v_add3_u32 v46, v46, v47, s42
	v_add3_u32 v62, v20, v63, s42
	v_add_u32_e32 v20, v66, v64
	v_lshl_add_u64 v[126:127], s[22:23], 0, v[18:19]
	v_add_u32_e32 v18, s36, v21
	v_lshl_or_b32 v135, v39, 4, v38
	ds_read_b128 v[42:45], v135
	v_ashrrev_i32_e32 v47, 31, v46
	v_add3_u32 v64, v20, v65, s42
	v_add_u32_e32 v136, 0xc000, v18
	v_add_u32_e32 v18, s37, v21
	s_load_dwordx2 s[12:13], s[0:1], 0x20
	ds_read_b128 v[38:41], v135 offset:2048
	v_lshlrev_b64 v[46:47], 7, v[46:47]
	v_ashrrev_i32_e32 v49, 31, v48
	v_ashrrev_i32_e32 v59, 31, v58
	v_ashrrev_i32_e32 v61, 31, v60
	v_ashrrev_i32_e32 v63, 31, v62
	v_ashrrev_i32_e32 v65, 31, v64
	v_add_u32_e32 v137, 0xc000, v18
	v_add_u32_e32 v18, s38, v21
	ds_read_b128 v[54:57], v132 offset:4096
	v_lshl_add_u64 v[46:47], s[20:21], 0, v[46:47]
	v_mov_b32_e32 v69, v19
	v_lshlrev_b64 v[48:49], 7, v[48:49]
	v_lshlrev_b64 v[58:59], 7, v[58:59]
	v_lshlrev_b64 v[60:61], 7, v[60:61]
	v_lshlrev_b64 v[62:63], 7, v[62:63]
	v_lshlrev_b64 v[64:65], 7, v[64:65]
	v_add_u32_e32 v138, 0xc000, v18
	v_add_u32_e32 v18, s39, v21
	ds_read_b128 v[50:53], v132 offset:6144
	v_lshl_add_u64 v[46:47], v[46:47], 0, v[68:69]
	v_lshl_add_u64 v[48:49], s[20:21], 0, v[48:49]
	v_lshl_add_u64 v[58:59], s[20:21], 0, v[58:59]
	v_lshl_add_u64 v[60:61], s[20:21], 0, v[60:61]
	v_lshl_add_u64 v[62:63], s[20:21], 0, v[62:63]
	v_lshl_add_u64 v[64:65], s[20:21], 0, v[64:65]
	v_mov_b32_e32 v20, s19
	v_add_u32_e32 v139, 0xc000, v18
	v_add_u32_e32 v18, s40, v21
	v_lshl_add_u64 v[48:49], v[48:49], 0, v[68:69]
	v_lshl_add_u64 v[58:59], v[58:59], 0, v[68:69]
	v_lshl_add_u64 v[60:61], v[60:61], 0, v[68:69]
	v_lshl_add_u64 v[62:63], v[62:63], 0, v[68:69]
	v_lshl_add_u64 v[64:65], v[64:65], 0, v[68:69]
	v_cndmask_b32_e32 v115, v20, v47, vcc
	v_mov_b32_e32 v47, s18
	v_add_u32_e32 v140, 0xc000, v18
	v_add_u32_e32 v18, s41, v21
	s_mov_b32 s30, 6
	v_xor_b32_e32 v133, 64, v132
	s_mov_b32 s31, 0
	s_mov_b32 s35, 1
	s_mov_b32 s34, 0xc000
	v_cndmask_b32_e32 v114, v47, v46, vcc
	v_cndmask_b32_e64 v117, v20, v49, s[2:3]
	v_cndmask_b32_e64 v116, v47, v48, s[2:3]
	v_cndmask_b32_e64 v119, v20, v59, s[4:5]
	v_cndmask_b32_e64 v118, v47, v58, s[4:5]
	v_cndmask_b32_e64 v121, v20, v61, s[6:7]
	v_cndmask_b32_e64 v120, v47, v60, s[6:7]
	v_cndmask_b32_e64 v123, v20, v63, s[8:9]
	v_cndmask_b32_e64 v122, v47, v62, s[8:9]
	v_cndmask_b32_e64 v125, v20, v65, s[10:11]
	v_cndmask_b32_e64 v124, v47, v64, s[10:11]
	s_mov_b64 s[2:3], 0
	v_add_u32_e32 v141, 0xc000, v18
	v_mov_b32_e32 v18, v19
	v_mov_b32_e32 v20, v19
	v_mov_b32_e32 v21, v19
	v_mov_b32_e32 v46, v19
	v_mov_b32_e32 v47, v19
	v_mov_b32_e32 v48, v19
	v_mov_b32_e32 v49, v19
	v_mov_b32_e32 v58, v19
	v_mov_b32_e32 v59, v19
	v_mov_b32_e32 v60, v19
	v_mov_b32_e32 v61, v19
	v_mov_b32_e32 v74, v19
	v_mov_b32_e32 v75, v19
	v_mov_b32_e32 v76, v19
	v_mov_b32_e32 v77, v19
	v_mov_b32_e32 v82, v19
	v_mov_b32_e32 v83, v19
	v_mov_b32_e32 v84, v19
	v_mov_b32_e32 v85, v19
	v_mov_b32_e32 v86, v19
	v_mov_b32_e32 v87, v19
	v_mov_b32_e32 v88, v19
	v_mov_b32_e32 v89, v19
	v_mov_b32_e32 v90, v19
	v_mov_b32_e32 v91, v19
	v_mov_b32_e32 v92, v19
	v_mov_b32_e32 v93, v19
	v_mov_b32_e32 v94, v19
	v_mov_b32_e32 v95, v19
	v_mov_b32_e32 v96, v19
	v_mov_b32_e32 v97, v19
	v_mov_b32_e32 v98, v19
	v_mov_b32_e32 v99, v19
	v_mov_b32_e32 v100, v19
	v_mov_b32_e32 v101, v19
	v_mov_b32_e32 v102, v19
	v_mov_b32_e32 v103, v19
	v_mov_b32_e32 v104, v19
	v_mov_b32_e32 v105, v19
	v_mov_b32_e32 v106, v19
	v_mov_b32_e32 v107, v19
	v_mov_b32_e32 v108, v19
	v_mov_b32_e32 v109, v19
	v_mov_b32_e32 v110, v19
	v_mov_b32_e32 v111, v19
	v_mov_b32_e32 v112, v19
	v_mov_b32_e32 v113, v19
	v_mov_b32_e32 v78, v19
	v_mov_b32_e32 v79, v19
	v_mov_b32_e32 v80, v19
	v_mov_b32_e32 v81, v19
	v_mov_b32_e32 v62, v19
	v_mov_b32_e32 v63, v19
	v_mov_b32_e32 v64, v19
	v_mov_b32_e32 v65, v19
	v_mov_b32_e32 v70, v19
	v_mov_b32_e32 v71, v19
	v_mov_b32_e32 v72, v19
	v_mov_b32_e32 v73, v19
	v_mov_b32_e32 v66, v19
	v_mov_b32_e32 v67, v19
	v_mov_b32_e32 v68, v19
	s_mov_b32 s60, 0
	s_add_i32 s63, s29, 2
	s_mul_i32 s73, s63, 11
	s_lshr_b32 s73, s73, 5
	s_mul_i32 s73, s73, 31
	s_add_i32 s62, s63, s73
	s_mov_b32 s64, 0
	s_mov_b32 s66, 1
	s_mov_b32 s67, 0
	s_add_i32 s75, s29, 6
	s_lshl_b32 s68, s75, 15
	s_mov_b32 s69, 0
	v_lshl_add_u64 v[178:179], v[126:127], 0, s[68:69]
	s_add_i32 s70, s33, 0xc000
	v_lshl_add_u64 v[180:181], v[178:179], 0, s[16:17]
	v_mov_b32_e32 v174, v133

_Z6conv_kILi256ELi512ELi3ELi128ELi1ELi1ELb0EEvPKDF16_S1_PKfS3_PDF16_S4_S1_fS3_S3_S3_S3_:
	s_lshl_b32 s3, s2, 3
	s_load_dwordx2 s[36:37], s[0:1], 0x0
	s_load_dwordx2 s[84:85], s[0:1], 0x8
	s_load_dwordx4 s[4:7], s[0:1], 0x10
	s_load_dwordx2 s[30:31], s[0:1], 0x30
	s_and_b32 s3, s3, 56
	s_ashr_i32 s8, s2, 5
	s_add_i32 s3, s3, s8
	v_readfirstlane_b32 s40, v0
	s_lshl_b32 s8, s3, 2
	s_bfe_u32 s49, s2, 0x20003
	s_and_b32 s33, s8, 56
	s_lshr_b32 s50, s40, 6
	s_bfe_u32 s41, s40, 0x10006
	s_ashr_i32 s38, s3, 4
	s_and_b32 s27, s2, 32
	s_lshl_b32 s2, s49, 9
	s_waitcnt lgkmcnt(0)
	s_add_u32 s2, s4, s2
	s_addc_u32 s3, s5, 0
	s_lshl_b32 s4, s41, 8
	s_add_u32 s2, s2, s4
	s_addc_u32 s3, s3, 0
	v_and_b32_e32 v18, 48, v0
	v_mov_b32_e32 v19, 0
	v_lshl_add_u64 v[2:3], s[2:3], 0, v[18:19]
	s_load_dword s26, s[6:7], 0x0
	global_load_dwordx4 v[14:17], v[2:3], off
	v_lshl_add_u64 v[4:5], v[2:3], 0, 64
	s_mov_b64 s[2:3], 0x80
	v_bfe_u32 v28, v0, 3, 3
	v_and_b32_e32 v1, 7, v0
	global_load_dwordx4 v[10:13], v[4:5], off
	v_lshl_add_u64 v[4:5], v[2:3], 0, s[2:3]
	s_mov_b64 s[2:3], 0xc0
	v_bitop3_b32 v1, v28, v1, 6 bitop3:0x6c
	v_lshl_add_u64 v[2:3], v[2:3], 0, s[2:3]
	v_lshl_or_b32 v18, s50, 3, v28
	s_mov_b32 s2, 0x1e1e1e1f
	v_lshlrev_b32_e32 v20, 3, v1
	v_mul_hi_u32 v1, v18, s2
	v_lshrrev_b32_e32 v21, 2, v1
	s_movk_i32 s8, 0xffde
	s_add_i32 s24, s33, -1
	global_load_dwordx4 v[6:9], v[4:5], off
	v_mul_lo_u32 v22, v21, s8
	v_add_u32_e32 v1, s24, v21
	s_add_i32 s25, s27, -1
	s_movk_i32 s9, 0x154
	global_load_dwordx4 v[2:5], v[2:3], off
	v_add3_u32 v24, s25, v18, v22
	v_cmp_gt_u32_e64 s[2:3], s9, v18
	v_cmp_gt_u32_e32 vcc, 64, v1
	s_and_b64 s[6:7], s[2:3], vcc
	v_cmp_gt_u32_e64 s[4:5], 64, v24
	v_and_b32_e32 v25, 63, v0
	s_and_b64 s[10:11], s[6:7], s[4:5]
	v_mov_b64_e32 v[22:23], s[30:31]
	v_lshlrev_b32_e32 v18, 1, v20
	s_and_saveexec_b64 s[6:7], s[10:11]
	s_lshl_b32 s10, s38, 14
	v_lshlrev_b32_e32 v1, 6, v1
	v_or3_b32 v22, v1, s10, v24
	v_ashrrev_i32_e32 v23, 31, v22
	v_lshlrev_b64 v[22:23], 7, v[22:23]
	v_lshl_add_u64 v[22:23], s[36:37], 0, v[22:23]
	v_lshl_add_u64 v[22:23], v[22:23], 0, v[18:19]
	s_or_b64 exec, exec, s[6:7]
	s_lshl_b32 s42, s50, 10
	v_lshlrev_b32_e32 v1, 4, v25
	v_or_b32_e32 v19, s42, v1
	s_add_i32 s13, s50, 8
	v_readfirstlane_b32 s6, v19
	s_mov_b32 m0, s6
	s_mov_b32 s12, 0x3c3c3c3d
	global_load_lds_dwordx4 v[22:23], off
	v_lshl_or_b32 v22, s13, 3, v28
	v_mul_hi_u32 v19, v22, s12
	v_lshrrev_b32_e32 v26, 3, v19
	v_mul_lo_u32 v23, v26, s8
	v_add_u32_e32 v19, s24, v26
	v_add3_u32 v27, s25, v22, v23
	v_cmp_gt_u32_e64 s[6:7], s9, v22
	v_cmp_gt_u32_e32 vcc, 64, v19
	s_and_b64 s[10:11], s[6:7], vcc
	v_cmp_gt_u32_e64 s[8:9], 64, v27
	s_and_b64 s[14:15], s[10:11], s[8:9]
	v_mov_b64_e32 v[22:23], s[30:31]
	s_and_saveexec_b64 s[10:11], s[14:15]
	s_lshl_b32 s14, s38, 14
	v_lshlrev_b32_e32 v19, 6, v19
	v_or3_b32 v22, v19, s14, v27
	v_ashrrev_i32_e32 v23, 31, v22
	v_lshlrev_b64 v[22:23], 7, v[22:23]
	v_lshl_add_u64 v[22:23], s[36:37], 0, v[22:23]
	v_mov_b32_e32 v19, 0
	v_lshl_add_u64 v[22:23], v[22:23], 0, v[18:19]
	s_or_b64 exec, exec, s[10:11]
	s_lshl_b32 s43, s13, 10
	v_or_b32_e32 v19, s43, v1
	s_add_i32 s18, s50, 16
	v_readfirstlane_b32 s10, v19
	s_mov_b32 m0, s10
	s_movk_i32 s16, 0xffde
	global_load_lds_dwordx4 v[22:23], off
	v_lshl_or_b32 v22, s18, 3, v28
	v_mul_hi_u32 v19, v22, s12
	v_lshrrev_b32_e32 v29, 3, v19
	v_mul_lo_u32 v23, v29, s16
	v_add_u32_e32 v19, s24, v29
	s_movk_i32 s17, 0x154
	v_add3_u32 v30, s25, v22, v23
	v_cmp_gt_u32_e64 s[10:11], s17, v22
	v_cmp_gt_u32_e32 vcc, 64, v19
	s_and_b64 s[14:15], s[10:11], vcc
	v_cmp_gt_u32_e64 s[12:13], 64, v30
	s_and_b64 s[20:21], s[14:15], s[12:13]
	v_mov_b64_e32 v[22:23], s[30:31]
	s_and_saveexec_b64 s[14:15], s[20:21]
	s_lshl_b32 s19, s38, 14
	v_lshlrev_b32_e32 v19, 6, v19
	v_or3_b32 v22, v19, s19, v30
	v_ashrrev_i32_e32 v23, 31, v22
	v_lshlrev_b64 v[22:23], 7, v[22:23]
	v_lshl_add_u64 v[22:23], s[36:37], 0, v[22:23]
	v_mov_b32_e32 v19, 0
	v_lshl_add_u64 v[22:23], v[22:23], 0, v[18:19]
	s_or_b64 exec, exec, s[14:15]
	s_lshl_b32 s44, s18, 10
	v_or_b32_e32 v19, s44, v1
	s_add_i32 s21, s50, 24
	v_readfirstlane_b32 s14, v19
	s_mov_b32 m0, s14
	s_mov_b32 s20, 0x3c3c3c3d
	global_load_lds_dwordx4 v[22:23], off
	v_lshl_or_b32 v22, s21, 3, v28
	v_mul_hi_u32 v19, v22, s20
	v_lshrrev_b32_e32 v31, 3, v19
	v_mul_lo_u32 v23, v31, s16
	v_add_u32_e32 v19, s24, v31
	v_add3_u32 v32, s25, v22, v23
	v_cmp_gt_u32_e64 s[14:15], s17, v22
	v_cmp_gt_u32_e32 vcc, 64, v19
	s_and_b64 s[18:19], s[14:15], vcc
	v_cmp_gt_u32_e64 s[16:17], 64, v32
	s_and_b64 s[22:23], s[18:19], s[16:17]
	v_mov_b64_e32 v[22:23], s[30:31]
	s_and_saveexec_b64 s[18:19], s[22:23]
	s_lshl_b32 s22, s38, 14
	v_lshlrev_b32_e32 v19, 6, v19
	v_or3_b32 v22, v19, s22, v32
	v_ashrrev_i32_e32 v23, 31, v22
	v_lshlrev_b64 v[22:23], 7, v[22:23]
	v_lshl_add_u64 v[22:23], s[36:37], 0, v[22:23]
	v_mov_b32_e32 v19, 0
	v_lshl_add_u64 v[22:23], v[22:23], 0, v[18:19]
	s_or_b64 exec, exec, s[18:19]
	s_lshl_b32 s45, s21, 10
	v_or_b32_e32 v19, s45, v1
	s_add_i32 s28, s50, 32
	v_readfirstlane_b32 s18, v19
	s_mov_b32 m0, s18
	s_movk_i32 s18, 0xffde
	global_load_lds_dwordx4 v[22:23], off
	v_lshl_or_b32 v22, s28, 3, v28
	v_mul_hi_u32 v19, v22, s20
	v_lshrrev_b32_e32 v33, 3, v19
	v_mul_lo_u32 v23, v33, s18
	v_add_u32_e32 v19, s24, v33
	s_movk_i32 s18, 0x154
	v_add3_u32 v34, s25, v22, v23
	v_cmp_gt_u32_e64 s[18:19], s18, v22
	v_cmp_gt_u32_e32 vcc, 64, v19
	s_and_b64 s[22:23], s[18:19], vcc
	v_cmp_gt_u32_e64 s[20:21], 64, v34
	s_and_b64 s[22:23], s[22:23], s[20:21]
	s_xor_b64 s[22:23], s[22:23], -1
	s_and_saveexec_b64 s[34:35], s[22:23]
	s_xor_b64 s[22:23], exec, s[34:35]
	s_lshl_b32 s29, s38, 14
	s_or_saveexec_b64 s[22:23], s[22:23]
	v_mov_b32_e32 v35, s29
	v_mov_b64_e32 v[22:23], s[30:31]
	s_xor_b64 exec, exec, s[22:23]
	s_lshl_b32 s29, s38, 14
	v_lshlrev_b32_e32 v19, 6, v19
	v_or3_b32 v22, v19, s29, v34
	v_ashrrev_i32_e32 v23, 31, v22
	v_lshlrev_b64 v[22:23], 7, v[22:23]
	v_lshl_add_u64 v[22:23], s[36:37], 0, v[22:23]
	v_mov_b32_e32 v19, 0
	v_lshl_add_u64 v[22:23], v[22:23], 0, v[18:19]
	v_mov_b32_e32 v35, s29
	s_or_b64 exec, exec, s[22:23]
	s_lshl_b32 s46, s28, 10
	v_or_b32_e32 v18, s46, v1
	s_add_i32 s48, s50, 40
	v_readfirstlane_b32 s22, v18
	s_mov_b32 m0, s22
	v_lshl_or_b32 v19, s48, 3, v28
	global_load_lds_dwordx4 v[22:23], off
	s_mov_b32 s22, 0x3c3c3c3d
	v_mul_hi_u32 v18, v19, s22
	v_lshrrev_b32_e32 v36, 3, v18
	s_movk_i32 s22, 0xffde
	s_mov_b64 s[34:35], s[84:85]
	v_mul_lo_u32 v22, v36, s22
	v_add_u32_e32 v18, s24, v36
	s_movk_i32 s22, 0x154
	v_add3_u32 v37, s25, v19, v22
	v_cmp_gt_u32_e64 s[22:23], s22, v19
	v_cmp_gt_u32_e32 vcc, 64, v18
	s_and_b64 s[28:29], s[22:23], vcc
	v_cmp_gt_u32_e64 s[24:25], 64, v37
	s_and_b64 s[28:29], s[28:29], s[24:25]
	s_xor_b64 s[28:29], s[28:29], -1
	s_and_saveexec_b64 s[52:53], s[28:29]
	s_xor_b64 s[28:29], exec, s[52:53]
	s_or_saveexec_b64 s[28:29], s[28:29]
	s_lshl_b32 s51, s41, 6
	v_mov_b64_e32 v[22:23], s[30:31]
	s_xor_b64 exec, exec, s[28:29]
	v_lshlrev_b32_e32 v18, 6, v18
	v_or3_b32 v18, v18, v35, v37
	v_ashrrev_i32_e32 v19, 31, v18
	v_lshlrev_b64 v[18:19], 7, v[18:19]
	v_lshl_add_u64 v[18:19], s[36:37], 0, v[18:19]
	v_lshlrev_b32_e32 v22, 1, v20
	v_mov_b32_e32 v23, 0
	v_lshl_add_u64 v[22:23], v[18:19], 0, v[22:23]
	s_or_b64 exec, exec, s[28:29]
	v_and_b32_e32 v114, 15, v0
	s_and_b32 s52, s50, 6
	v_mad_u64_u32 v[116:117], s[52:53], s52, 34, v[114:115]
	v_lshrrev_b32_e32 v115, 4, v25
	v_or_b32_e32 v19, s51, v114
	v_bitop3_b32 v25, v115, v0, 6 bitop3:0x78
	v_lshlrev_b32_e32 v19, 7, v19
	v_lshlrev_b32_e32 v25, 4, v25
	s_mov_b32 s51, 0x18040
	s_lshl_b32 s48, s48, 10
	v_lshlrev_b32_e32 v18, 6, v28
	v_or_b32_e32 v28, v19, v25
	v_bitop3_b32 v125, v19, s51, v25 bitop3:0x36
	v_or_b32_e32 v19, s48, v1
	s_lshl_b32 s39, s49, 7
	v_readfirstlane_b32 s51, v19
	s_lshr_b32 s47, s40, 7
	s_mov_b32 m0, s51
	s_lshl_b32 s51, s49, 14
	s_waitcnt lgkmcnt(0)
	s_add_u32 s52, s34, s51
	v_or3_b32 v18, s42, v18, v20
	s_addc_u32 s53, s35, 0
	s_lshl_b32 s56, s50, 11
	v_mov_b32_e32 v19, 0
	global_load_lds_dwordx4 v[22:23], off
	s_add_i32 s50, s56, 0x18000
	v_lshlrev_b64 v[22:23], 1, v[18:19]
	v_lshl_add_u64 v[118:119], s[52:53], 0, v[22:23]
	s_mov_b32 m0, s50
	s_mov_b64 s[34:35], 0x400
	global_load_lds_dwordx4 v[118:119], off
	s_add_i32 m0, s56, 0x18400
	s_add_u32 s54, s52, 0x30000
	v_lshl_add_u64 v[40:41], v[118:119], 0, s[34:35]
	s_addc_u32 s55, s53, 0
	global_load_lds_dwordx4 v[40:41], off
	s_add_i32 m0, s56, 0x1c000
	v_lshl_add_u64 v[40:41], s[54:55], 0, v[22:23]
	v_or_b32_e32 v38, 0x200, v18
	v_mov_b32_e32 v39, v19
	global_load_lds_dwordx4 v[40:41], off
	s_add_i32 m0, s56, 0x1c400
	v_lshlrev_b64 v[38:39], 1, v[38:39]
	s_add_u32 s52, s52, 0x60000
	v_lshl_add_u64 v[40:41], s[54:55], 0, v[38:39]
	s_addc_u32 s53, s53, 0
	global_load_lds_dwordx4 v[40:41], off
	s_add_i32 m0, s56, 0x20000
	v_lshl_add_u64 v[22:23], s[52:53], 0, v[22:23]
	global_load_lds_dwordx4 v[22:23], off
	v_lshl_add_u64 v[22:23], s[52:53], 0, v[38:39]
	s_add_i32 m0, s56, 0x20400
	v_or_b32_e32 v124, 0x18000, v28
	global_load_lds_dwordx4 v[22:23], off
	s_waitcnt vmcnt(4) lgkmcnt(0)
	s_barrier
	ds_read_b128 v[66:69], v124
	ds_read_b128 v[70:73], v124 offset:2048
	v_lshlrev_b32_e32 v18, 7, v116
	v_bitop3_b32 v22, v116, v115, 6 bitop3:0x6c
	v_add_u32_e32 v117, 34, v116
	v_lshl_or_b32 v138, v22, 4, v18
	ds_read_b128 v[78:81], v138
	ds_read_b128 v[74:77], v138 offset:2048
	v_lshlrev_b32_e32 v18, 7, v117
	v_bitop3_b32 v22, v117, v115, 6 bitop3:0x6c
	v_lshl_or_b32 v139, v22, 4, v18
	ds_read_b128 v[82:85], v139
	s_load_dwordx2 s[28:29], s[0:1], 0x20
	ds_read_b128 v[86:89], v139 offset:2048
	ds_read_b128 v[94:97], v124 offset:4096
	ds_read_b128 v[98:101], v124 offset:6144
	v_lshlrev_b32_e32 v18, 1, v20
	s_mov_b32 s49, 0
	s_mov_b32 s51, 1
	v_add_u32_e32 v126, s33, v21
	v_add_u32_e32 v127, v35, v24
	v_lshl_add_u64 v[120:121], s[36:37], 0, v[18:19]
	v_add_u32_e32 v128, s33, v26
	v_add_u32_e32 v129, v35, v27
	v_add_u32_e32 v130, s33, v29
	v_add_u32_e32 v131, v35, v30
	v_add_u32_e32 v132, s33, v31
	v_add_u32_e32 v133, v35, v32
	v_add_u32_e32 v134, s33, v33
	v_add_u32_e32 v135, v35, v34
	v_add_u32_e32 v136, s33, v36
	v_add_u32_e32 v137, v35, v37
	s_mov_b64 s[36:37], 0
	s_mov_b32 s52, 0
	v_mov_b32_e32 v18, v19
	v_mov_b32_e32 v20, v19
	v_mov_b32_e32 v21, v19
	v_mov_b32_e32 v38, v19
	v_mov_b32_e32 v39, v19
	v_mov_b32_e32 v40, v19
	v_mov_b32_e32 v41, v19
	v_mov_b32_e32 v42, v19
	v_mov_b32_e32 v43, v19
	v_mov_b32_e32 v44, v19
	v_mov_b32_e32 v45, v19
	v_mov_b32_e32 v46, v19
	v_mov_b32_e32 v47, v19
	v_mov_b32_e32 v48, v19
	v_mov_b32_e32 v49, v19
	v_mov_b32_e32 v50, v19
	v_mov_b32_e32 v51, v19
	v_mov_b32_e32 v52, v19
	v_mov_b32_e32 v53, v19
	v_mov_b32_e32 v54, v19
	v_mov_b32_e32 v55, v19
	v_mov_b32_e32 v56, v19
	v_mov_b32_e32 v57, v19
	v_mov_b32_e32 v58, v19
	v_mov_b32_e32 v59, v19
	v_mov_b32_e32 v60, v19
	v_mov_b32_e32 v61, v19
	v_mov_b32_e32 v62, v19
	v_mov_b32_e32 v63, v19
	v_mov_b32_e32 v64, v19
	v_mov_b32_e32 v65, v19
	v_mov_b32_e32 v90, v19
	v_mov_b32_e32 v91, v19
	v_mov_b32_e32 v92, v19
	v_mov_b32_e32 v93, v19
	v_mov_b32_e32 v102, v19
	v_mov_b32_e32 v103, v19
	v_mov_b32_e32 v104, v19
	v_mov_b32_e32 v105, v19
	v_mov_b32_e32 v106, v19
	v_mov_b32_e32 v107, v19
	v_mov_b32_e32 v108, v19
	v_mov_b32_e32 v109, v19
	v_mov_b32_e32 v110, v19
	v_mov_b32_e32 v111, v19
	v_mov_b32_e32 v112, v19
	v_mov_b32_e32 v113, v19
	v_mov_b32_e32 v34, v19
	v_mov_b32_e32 v35, v19
	v_mov_b32_e32 v36, v19
	v_mov_b32_e32 v37, v19
	v_mov_b32_e32 v30, v19
	v_mov_b32_e32 v31, v19
	v_mov_b32_e32 v32, v19
	v_mov_b32_e32 v33, v19
	v_mov_b32_e32 v26, v19
	v_mov_b32_e32 v27, v19
	v_mov_b32_e32 v28, v19
	v_mov_b32_e32 v29, v19
	v_mov_b32_e32 v22, v19
	v_mov_b32_e32 v23, v19
	v_mov_b32_e32 v24, v19
	v_mov_b32_e32 v25, v19
	s_mov_b32 s60, 0
	s_mov_b32 s61, 0
	s_mov_b32 s62, 0
	s_mov_b32 s64, 0
	s_mov_b32 s66, 1
	s_mov_b32 s67, 0
	s_mov_b32 s69, 0
	v_mov_b32_e32 v172, v125
	s_waitcnt lgkmcnt(0)

_Z6conv_kILi512ELi256ELi3ELi64ELi1ELi1ELb0EEvPKDF16_S1_PKfS3_PDF16_S4_S1_fS3_S3_S3_S3_:
	s_lshl_b32 s3, s2, 3
	s_load_dwordx2 s[36:37], s[0:1], 0x0
	s_load_dwordx2 s[84:85], s[0:1], 0x8
	s_load_dwordx4 s[4:7], s[0:1], 0x10
	s_load_dwordx2 s[30:31], s[0:1], 0x30
	s_and_b32 s3, s3, 56
	s_ashr_i32 s8, s2, 5
	s_add_i32 s3, s3, s8
	v_readfirstlane_b32 s42, v0
	s_lshl_b32 s8, s3, 2
	s_bfe_u32 s38, s2, 0x20003
	s_and_b32 s33, s8, 56
	s_lshr_b32 s52, s42, 6
	s_ashr_i32 s40, s3, 4
	s_and_b32 s27, s2, 32
	s_lshl_b32 s2, s38, 8
	v_bfe_u32 v29, v0, 3, 3
	v_and_b32_e32 v2, 7, v0
	s_waitcnt lgkmcnt(0)
	s_add_u32 s2, s4, s2
	v_bitop3_b32 v2, v29, v2, 6 bitop3:0x6c
	s_addc_u32 s3, s5, 0
	v_and_b32_e32 v18, 48, v0
	v_mov_b32_e32 v19, 0
	v_lshlrev_b32_e32 v20, 3, v2
	v_lshl_add_u64 v[2:3], s[2:3], 0, v[18:19]
	s_load_dword s26, s[6:7], 0x0
	global_load_dwordx4 v[14:17], v[2:3], off
	v_lshl_add_u64 v[4:5], v[2:3], 0, 64
	s_mov_b64 s[2:3], 0x80
	global_load_dwordx4 v[10:13], v[4:5], off
	v_lshl_add_u64 v[4:5], v[2:3], 0, s[2:3]
	s_mov_b64 s[2:3], 0xc0
	v_lshl_add_u64 v[2:3], v[2:3], 0, s[2:3]
	v_lshl_or_b32 v18, s52, 3, v29
	s_mov_b32 s2, 0x1e1e1e1f
	v_mul_hi_u32 v21, v18, s2
	v_lshrrev_b32_e32 v21, 2, v21
	s_movk_i32 s8, 0xffde
	s_add_i32 s24, s33, -1
	global_load_dwordx4 v[6:9], v[4:5], off
	v_mul_lo_u32 v22, v21, s8
	v_add_u32_e32 v25, s24, v21
	s_add_i32 s25, s27, -1
	s_movk_i32 s9, 0x154
	global_load_dwordx4 v[2:5], v[2:3], off
	v_add3_u32 v24, s25, v18, v22
	v_cmp_gt_u32_e64 s[2:3], s9, v18
	v_cmp_gt_u32_e32 vcc, 64, v25
	s_and_b64 s[6:7], s[2:3], vcc
	v_cmp_gt_u32_e64 s[4:5], 64, v24
	v_and_b32_e32 v1, 63, v0
	s_and_b64 s[10:11], s[6:7], s[4:5]
	v_mov_b64_e32 v[22:23], s[30:31]
	v_lshlrev_b32_e32 v18, 1, v20
	s_and_saveexec_b64 s[6:7], s[10:11]
	s_lshl_b32 s10, s40, 15
	v_lshlrev_b32_e32 v22, 6, v25
	v_or3_b32 v22, v22, s10, v24
	v_ashrrev_i32_e32 v23, 31, v22
	v_lshlrev_b64 v[22:23], 7, v[22:23]
	v_lshl_add_u64 v[22:23], s[36:37], 0, v[22:23]
	v_lshl_add_u64 v[22:23], v[22:23], 0, v[18:19]
	s_or_b64 exec, exec, s[6:7]
	s_lshl_b32 s43, s52, 10
	v_lshlrev_b32_e32 v120, 4, v1
	v_or_b32_e32 v19, s43, v120
	s_add_i32 s13, s52, 8
	v_readfirstlane_b32 s6, v19
	s_mov_b32 m0, s6
	s_mov_b32 s12, 0x3c3c3c3d
	v_mov_b64_e32 v[184:185], v[22:23]
	global_load_lds_dwordx4 v[22:23], off
	v_lshl_or_b32 v22, s13, 3, v29
	v_mul_hi_u32 v19, v22, s12
	v_lshrrev_b32_e32 v25, 3, v19
	v_mul_lo_u32 v23, v25, s8
	v_add_u32_e32 v19, s24, v25
	v_add3_u32 v26, s25, v22, v23
	v_cmp_gt_u32_e64 s[6:7], s9, v22
	v_cmp_gt_u32_e32 vcc, 64, v19
	s_and_b64 s[10:11], s[6:7], vcc
	v_cmp_gt_u32_e64 s[8:9], 64, v26
	s_and_b64 s[14:15], s[10:11], s[8:9]
	v_mov_b64_e32 v[22:23], s[30:31]
	s_and_saveexec_b64 s[10:11], s[14:15]
	s_lshl_b32 s14, s40, 15
	v_lshlrev_b32_e32 v19, 6, v19
	v_or3_b32 v22, v19, s14, v26
	v_ashrrev_i32_e32 v23, 31, v22
	v_lshlrev_b64 v[22:23], 7, v[22:23]
	v_lshl_add_u64 v[22:23], s[36:37], 0, v[22:23]
	v_mov_b32_e32 v19, 0
	v_lshl_add_u64 v[22:23], v[22:23], 0, v[18:19]
	s_or_b64 exec, exec, s[10:11]
	s_lshl_b32 s44, s13, 10
	v_or_b32_e32 v19, s44, v120
	s_add_i32 s18, s52, 16
	v_readfirstlane_b32 s10, v19
	s_mov_b32 m0, s10
	s_movk_i32 s16, 0xffde
	v_mov_b64_e32 v[186:187], v[22:23]
	global_load_lds_dwordx4 v[22:23], off
	v_lshl_or_b32 v22, s18, 3, v29
	v_mul_hi_u32 v19, v22, s12
	v_lshrrev_b32_e32 v27, 3, v19
	v_mul_lo_u32 v23, v27, s16
	v_add_u32_e32 v19, s24, v27
	s_movk_i32 s17, 0x154
	v_add3_u32 v28, s25, v22, v23
	v_cmp_gt_u32_e64 s[10:11], s17, v22
	v_cmp_gt_u32_e32 vcc, 64, v19
	s_and_b64 s[14:15], s[10:11], vcc
	v_cmp_gt_u32_e64 s[12:13], 64, v28
	s_and_b64 s[20:21], s[14:15], s[12:13]
	v_mov_b64_e32 v[22:23], s[30:31]
	s_and_saveexec_b64 s[14:15], s[20:21]
	s_lshl_b32 s19, s40, 15
	v_lshlrev_b32_e32 v19, 6, v19
	v_or3_b32 v22, v19, s19, v28
	v_ashrrev_i32_e32 v23, 31, v22
	v_lshlrev_b64 v[22:23], 7, v[22:23]
	v_lshl_add_u64 v[22:23], s[36:37], 0, v[22:23]
	v_mov_b32_e32 v19, 0
	v_lshl_add_u64 v[22:23], v[22:23], 0, v[18:19]
	s_or_b64 exec, exec, s[14:15]
	s_lshl_b32 s45, s18, 10
	v_or_b32_e32 v19, s45, v120
	s_add_i32 s21, s52, 24
	v_readfirstlane_b32 s14, v19
	s_mov_b32 m0, s14
	s_mov_b32 s20, 0x3c3c3c3d
	v_mov_b64_e32 v[188:189], v[22:23]
	global_load_lds_dwordx4 v[22:23], off
	v_lshl_or_b32 v22, s21, 3, v29
	v_mul_hi_u32 v19, v22, s20
	v_lshrrev_b32_e32 v30, 3, v19
	v_mul_lo_u32 v23, v30, s16
	v_add_u32_e32 v19, s24, v30
	v_add3_u32 v31, s25, v22, v23
	v_cmp_gt_u32_e64 s[14:15], s17, v22
	v_cmp_gt_u32_e32 vcc, 64, v19
	s_and_b64 s[18:19], s[14:15], vcc
	v_cmp_gt_u32_e64 s[16:17], 64, v31
	s_and_b64 s[22:23], s[18:19], s[16:17]
	v_mov_b64_e32 v[22:23], s[30:31]
	s_and_saveexec_b64 s[18:19], s[22:23]
	s_lshl_b32 s22, s40, 15
	v_lshlrev_b32_e32 v19, 6, v19
	v_or3_b32 v22, v19, s22, v31
	v_ashrrev_i32_e32 v23, 31, v22
	v_lshlrev_b64 v[22:23], 7, v[22:23]
	v_lshl_add_u64 v[22:23], s[36:37], 0, v[22:23]
	v_mov_b32_e32 v19, 0
	v_lshl_add_u64 v[22:23], v[22:23], 0, v[18:19]
	s_or_b64 exec, exec, s[18:19]
	s_lshl_b32 s46, s21, 10
	v_or_b32_e32 v19, s46, v120
	s_add_i32 s28, s52, 32
	v_readfirstlane_b32 s18, v19
	s_mov_b32 m0, s18
	s_movk_i32 s18, 0xffde
	v_mov_b64_e32 v[190:191], v[22:23]
	global_load_lds_dwordx4 v[22:23], off
	v_lshl_or_b32 v22, s28, 3, v29
	v_mul_hi_u32 v19, v22, s20
	v_lshrrev_b32_e32 v32, 3, v19
	v_mul_lo_u32 v23, v32, s18
	v_add_u32_e32 v19, s24, v32
	s_movk_i32 s18, 0x154
	v_add3_u32 v33, s25, v22, v23
	v_cmp_gt_u32_e64 s[18:19], s18, v22
	v_cmp_gt_u32_e32 vcc, 64, v19
	s_and_b64 s[22:23], s[18:19], vcc
	v_cmp_gt_u32_e64 s[20:21], 64, v33
	s_and_b64 s[22:23], s[22:23], s[20:21]
	s_xor_b64 s[22:23], s[22:23], -1
	s_and_saveexec_b64 s[34:35], s[22:23]
	s_xor_b64 s[22:23], exec, s[34:35]
	s_lshl_b32 s29, s40, 15
	s_or_saveexec_b64 s[22:23], s[22:23]
	v_mov_b32_e32 v34, s29
	v_mov_b64_e32 v[22:23], s[30:31]
	s_xor_b64 exec, exec, s[22:23]
	s_lshl_b32 s29, s40, 15
	v_lshlrev_b32_e32 v19, 6, v19
	v_or3_b32 v22, v19, s29, v33
	v_ashrrev_i32_e32 v23, 31, v22
	v_lshlrev_b64 v[22:23], 7, v[22:23]
	v_lshl_add_u64 v[22:23], s[36:37], 0, v[22:23]
	v_mov_b32_e32 v19, 0
	v_lshl_add_u64 v[22:23], v[22:23], 0, v[18:19]
	v_mov_b32_e32 v34, s29
	s_or_b64 exec, exec, s[22:23]
	s_lshl_b32 s47, s28, 10
	v_or_b32_e32 v18, s47, v120
	s_add_i32 s39, s52, 40
	v_readfirstlane_b32 s22, v18
	s_mov_b32 m0, s22
	v_lshl_or_b32 v18, s39, 3, v29
	v_mov_b64_e32 v[192:193], v[22:23]
	global_load_lds_dwordx4 v[22:23], off
	s_mov_b32 s22, 0x3c3c3c3d
	v_mul_hi_u32 v19, v18, s22
	v_lshrrev_b32_e32 v22, 3, v19
	s_movk_i32 s22, 0xffde
	s_mov_b64 s[34:35], s[84:85]
	v_mul_lo_u32 v19, v22, s22
	v_add_u32_e32 v35, s24, v22
	s_movk_i32 s22, 0x154
	v_add3_u32 v23, s25, v18, v19
	v_cmp_gt_u32_e64 s[22:23], s22, v18
	v_cmp_gt_u32_e32 vcc, 64, v35
	s_and_b64 s[28:29], s[22:23], vcc
	v_cmp_gt_u32_e64 s[24:25], 64, v23
	s_and_b64 s[28:29], s[28:29], s[24:25]
	s_xor_b64 s[28:29], s[28:29], -1
	s_and_saveexec_b64 s[48:49], s[28:29]
	s_xor_b64 s[28:29], exec, s[48:49]
	s_or_saveexec_b64 s[28:29], s[28:29]
	v_mov_b64_e32 v[18:19], s[30:31]
	s_xor_b64 exec, exec, s[28:29]
	v_lshlrev_b32_e32 v18, 6, v35
	v_or3_b32 v18, v18, v34, v23
	v_ashrrev_i32_e32 v19, 31, v18
	v_lshlrev_b64 v[18:19], 7, v[18:19]
	v_lshl_add_u64 v[18:19], s[36:37], 0, v[18:19]
	v_lshlrev_b32_e32 v36, 1, v20
	v_mov_b32_e32 v37, 0
	v_lshl_add_u64 v[18:19], v[18:19], 0, v[36:37]
	s_or_b64 exec, exec, s[28:29]
	v_lshrrev_b32_e32 v122, 4, v1
	v_bitop3_b32 v35, v122, v0, 6 bitop3:0x78
	s_and_b32 s48, s52, 3
	v_lshl_or_b32 v29, v29, 6, s43
	s_movk_i32 s50, 0xdc0
	v_and_b32_e32 v121, 15, v0
	v_lshlrev_b32_e32 v35, 4, v35
	s_lshr_b32 s49, s42, 8
	v_and_or_b32 v29, v29, s50, v20
	s_mul_i32 s50, s48, 0x44
	v_lshl_or_b32 v35, v121, 7, v35
	v_add_u32_e32 v123, s50, v121
	v_lshl_or_b32 v35, s49, 13, v35
	s_lshl_b32 s50, s39, 10
	s_lshl_b32 s41, s38, 6
	v_add_u32_e32 v125, 0x18000, v35
	v_or_b32_e32 v35, s50, v120
	s_lshl_b32 s38, s38, 13
	v_readfirstlane_b32 s39, v35
	s_waitcnt lgkmcnt(0)
	s_add_u32 s38, s34, s38
	s_mul_hi_u32 s57, s42, 0x38e38e39
	s_mov_b32 m0, s39
	s_addc_u32 s39, s35, 0
	s_lshr_b32 s34, s57, 12
	s_mulk_i32 s34, 0xffc1
	s_add_i32 s34, s34, s49
	s_mul_i32 s34, s49, 3
	s_lshl_b32 s56, s52, 11
	s_ashr_i32 s35, s34, 31
	s_add_i32 s52, s56, 0x18000
	s_lshl_b64 s[34:35], s[34:35], 15
	s_add_u32 s34, s38, s34
	s_addc_u32 s35, s39, s35
	s_mul_i32 s54, s49, -5
	s_add_i32 s54, s54, 6
	s_mul_hi_u32 s55, s54, 0x38e38e4
	s_mulk_i32 s55, 0xffc1
	s_add_i32 s54, s55, s54
	v_mov_b64_e32 v[194:195], v[18:19]
	global_load_lds_dwordx4 v[18:19], off
	v_lshlrev_b32_e32 v18, 1, v29
	v_mov_b32_e32 v19, 0
	s_mov_b32 m0, s52
	s_ashr_i32 s55, s54, 31
	v_lshl_add_u64 v[36:37], s[34:35], 0, v[18:19]
	global_load_lds_dwordx4 v18, s[34:35]
	s_mov_b64 s[34:35], 0x400
	s_add_i32 m0, s56, 0x18400
	s_lshl_b64 s[54:55], s[54:55], 15
	v_lshl_add_u64 v[36:37], v[36:37], 0, s[34:35]
	s_add_u32 s54, s38, s54
	global_load_lds_dwordx4 v[36:37], off
	s_addc_u32 s55, s39, s55
	s_add_i32 m0, s56, 0x1c000
	v_lshl_add_u64 v[36:37], s[54:55], 0, v[18:19]
	global_load_lds_dwordx4 v18, s[54:55]
	s_mul_i32 s54, s49, 3
	s_add_i32 s54, s54, 4
	s_mul_hi_u32 s55, s54, 0x38e38e4
	s_mulk_i32 s55, 0xffc1
	s_add_i32 s54, s55, s54
	s_ashr_i32 s55, s54, 31
	s_add_i32 m0, s56, 0x1c400
	s_lshl_b64 s[54:55], s[54:55], 15
	s_add_u32 s54, s38, s54
	v_lshl_add_u64 v[36:37], v[36:37], 0, s[34:35]
	s_addc_u32 s55, s39, s55
	global_load_lds_dwordx4 v[36:37], off
	s_add_i32 m0, s56, 0x20000
	v_lshl_add_u64 v[36:37], s[54:55], 0, v[18:19]
	global_load_lds_dwordx4 v18, s[54:55]
	v_lshl_add_u64 v[36:37], v[36:37], 0, s[34:35]
	s_add_i32 m0, s56, 0x20400
	s_lshr_b32 s54, s57, 9
	global_load_lds_dwordx4 v[36:37], off
	s_mul_i32 s54, s54, -9
	s_add_i32 s54, s54, s49
	s_mul_hi_i32 s55, s54, 0x55555556
	s_lshr_b32 s56, s55, 31
	s_add_i32 s55, s55, s56
	s_mul_i32 s55, s55, 31
	s_add_i32 s55, s55, s54
	s_bitcmp1_b32 s57, 9
	s_waitcnt vmcnt(4) lgkmcnt(0)
	s_barrier
	s_cselect_b32 s54, 0xc000, 0
	ds_read_b128 v[62:65], v125
	v_add_u32_e32 v29, s55, v123
	v_add_u32_e32 v124, 34, v123
	ds_read_b128 v[58:61], v125 offset:2048
	v_bitop3_b32 v35, v29, v122, 6 bitop3:0x6c
	v_lshl_add_u32 v29, v29, 7, s54
	v_lshl_or_b32 v139, v35, 4, v29
	ds_read_b128 v[70:73], v139
	v_add_u32_e32 v29, s55, v124
	ds_read_b128 v[66:69], v139 offset:2048
	v_bitop3_b32 v35, v29, v122, 6 bitop3:0x6c
	v_lshl_add_u32 v29, v29, 7, s54
	v_lshl_or_b32 v140, v35, 4, v29
	ds_read_b128 v[82:85], v140
	s_load_dwordx2 s[28:29], s[0:1], 0x20
	ds_read_b128 v[78:81], v140 offset:2048
	ds_read_b128 v[90:93], v125 offset:4096
	ds_read_b128 v[86:89], v125 offset:6144
	v_add_u32_e32 v127, s33, v21
	v_lshlrev_b32_e32 v20, 1, v20
	v_mov_b32_e32 v21, v19
	v_xor_b32_e32 v126, 64, v125
	s_mov_b32 s51, 0
	s_mov_b32 s53, 1
	v_add_u32_e32 v128, v34, v24
	v_lshl_add_u64 v[114:115], s[36:37], 0, v[20:21]
	v_add_u32_e32 v129, s33, v25
	v_add_u32_e32 v130, v34, v26
	v_add_u32_e32 v131, s33, v27
	v_add_u32_e32 v132, v34, v28
	v_add_u32_e32 v133, s33, v30
	v_add_u32_e32 v134, v34, v31
	v_add_u32_e32 v135, s33, v32
	v_add_u32_e32 v136, v34, v33
	v_add_u32_e32 v137, s33, v22
	v_add_u32_e32 v138, v34, v23
	v_lshl_add_u64 v[116:117], s[38:39], 0, v[18:19]
	s_mov_b64 s[36:37], 0
	s_mov_b32 s38, 0
	s_mov_b32 s39, 0
	v_mov_b32_e32 v18, v19
	v_mov_b32_e32 v20, v19
	v_mov_b32_e32 v22, v19
	v_mov_b32_e32 v23, v19
	v_mov_b32_e32 v24, v19
	v_mov_b32_e32 v25, v19
	v_mov_b32_e32 v26, v19
	v_mov_b32_e32 v27, v19
	v_mov_b32_e32 v28, v19
	v_mov_b32_e32 v29, v19
	v_mov_b32_e32 v42, v19
	v_mov_b32_e32 v43, v19
	v_mov_b32_e32 v44, v19
	v_mov_b32_e32 v45, v19
	v_mov_b32_e32 v50, v19
	v_mov_b32_e32 v51, v19
	v_mov_b32_e32 v52, v19
	v_mov_b32_e32 v53, v19
	v_mov_b32_e32 v54, v19
	v_mov_b32_e32 v55, v19
	v_mov_b32_e32 v56, v19
	v_mov_b32_e32 v57, v19
	v_mov_b32_e32 v74, v19
	v_mov_b32_e32 v75, v19
	v_mov_b32_e32 v76, v19
	v_mov_b32_e32 v77, v19
	v_mov_b32_e32 v94, v19
	v_mov_b32_e32 v95, v19
	v_mov_b32_e32 v96, v19
	v_mov_b32_e32 v97, v19
	v_mov_b32_e32 v98, v19
	v_mov_b32_e32 v99, v19
	v_mov_b32_e32 v100, v19
	v_mov_b32_e32 v101, v19
	v_mov_b32_e32 v102, v19
	v_mov_b32_e32 v103, v19
	v_mov_b32_e32 v104, v19
	v_mov_b32_e32 v105, v19
	v_mov_b32_e32 v106, v19
	v_mov_b32_e32 v107, v19
	v_mov_b32_e32 v108, v19
	v_mov_b32_e32 v109, v19
	v_mov_b32_e32 v110, v19
	v_mov_b32_e32 v111, v19
	v_mov_b32_e32 v112, v19
	v_mov_b32_e32 v113, v19
	v_mov_b32_e32 v46, v19
	v_mov_b32_e32 v47, v19
	v_mov_b32_e32 v48, v19
	v_mov_b32_e32 v49, v19
	v_mov_b32_e32 v30, v19
	v_mov_b32_e32 v31, v19
	v_mov_b32_e32 v32, v19
	v_mov_b32_e32 v33, v19
	v_mov_b32_e32 v38, v19
	v_mov_b32_e32 v39, v19
	v_mov_b32_e32 v40, v19
	v_mov_b32_e32 v41, v19
	v_mov_b32_e32 v34, v19
	v_mov_b32_e32 v35, v19
	v_mov_b32_e32 v36, v19
	v_mov_b32_e32 v37, v19
	v_mov_b32_e32 v202, 0x80000
	v_cmp_ne_u64_e64 s[76:77], v[184:185], s[30:31]
	s_nop 1
	v_cndmask_b32_e64 v196, 0, v202, s[76:77]
	v_cmp_ne_u64_e64 s[76:77], v[186:187], s[30:31]
	s_nop 1
	v_cndmask_b32_e64 v197, 0, v202, s[76:77]
	v_cmp_ne_u64_e64 s[76:77], v[188:189], s[30:31]
	s_nop 1
	v_cndmask_b32_e64 v198, 0, v202, s[76:77]
	v_cmp_ne_u64_e64 s[76:77], v[190:191], s[30:31]
	s_nop 1
	v_cndmask_b32_e64 v199, 0, v202, s[76:77]
	v_cmp_ne_u64_e64 s[76:77], v[192:193], s[30:31]
	s_nop 1
	v_cndmask_b32_e64 v200, 0, v202, s[76:77]
	v_cmp_ne_u64_e64 s[76:77], v[194:195], s[30:31]
	s_nop 1
	v_cndmask_b32_e64 v201, 0, v202, s[76:77]
	s_mov_b32 s61, 0
	s_mov_b32 s78, 0
	s_mov_b32 s67, 0
	s_mov_b32 s69, 0
	s_mov_b32 s80, 0xc000
	s_lshl_b32 s81, s49, 6
	s_lshl_b32 s79, s49, 13
	v_subrev_u32_e32 v204, s79, v125
	v_xor_b32_e32 v204, s81, v204
	v_add_u32_e32 v205, 0x2000, v204
	v_mov_b32_e32 v174, v205
	v_mov_b32_e32 v182, v123
	v_bitop3_b32 v183, v182, v122, 6 bitop3:0x6c
	v_lshl_add_u32 v182, v182, 7, 0
	v_lshl_or_b32 v176, v183, 4, v182
	v_xor_b32_e32 v176, s81, v176
	v_add_u32_e32 v182, 34, v123
	v_bitop3_b32 v183, v182, v122, 6 bitop3:0x6c
	v_lshl_add_u32 v182, v182, 7, 0
	v_lshl_or_b32 v177, v183, 4, v182
	v_xor_b32_e32 v177, s81, v177
	ds_read_b128 v[62:65], v204
	ds_read_b128 v[58:61], v204 offset:2048
	ds_read_b128 v[90:93], v204 offset:4096
	ds_read_b128 v[86:89], v204 offset:6144
	ds_read_b128 v[70:73], v176
	ds_read_b128 v[66:69], v176 offset:2048
	ds_read_b128 v[82:85], v177
	ds_read_b128 v[78:81], v177 offset:2048
	s_waitcnt lgkmcnt(0)

_Z6conv_kILi256ELi128ELi3ELi64ELi1ELi2ELb0EEvPKDF16_S1_PKfS3_PDF16_S4_S1_fS3_S3_S3_S3_:
	s_lshl_b32 s3, s2, 3
	s_and_b32 s3, s3, 56
	s_ashr_i32 s4, s2, 5
	s_add_i32 s4, s3, s4
	v_readfirstlane_b32 s28, v0
	v_bfe_u32 v8, v0, 3, 3
	s_lshl_b32 s3, s4, 2
	v_and_b32_e32 v1, 7, v0
	s_and_b32 s24, s3, 56
	s_lshr_b32 s3, s28, 6
	v_bitop3_b32 v2, v8, v1, 6 bitop3:0x6c
	s_ashr_i32 s26, s4, 4
	v_lshlrev_b32_e32 v4, 3, v2
	v_lshl_or_b32 v2, s3, 3, v8
	s_mov_b32 s4, 0x1e1e1e1f
	s_load_dwordx2 s[18:19], s[0:1], 0x0
	s_load_dwordx2 s[84:85], s[0:1], 0x8
	s_load_dwordx2 s[86:87], s[0:1], 0x28
	s_load_dwordx2 s[16:17], s[0:1], 0x30
	v_mul_hi_u32 v3, v2, s4
	s_and_b32 s25, s2, 32
	v_lshrrev_b32_e32 v3, 2, v3
	s_movk_i32 s6, 0xffde
	s_add_i32 s14, s24, -1
	v_mul_lo_u32 v5, v3, s6
	v_add_u32_e32 v30, s14, v3
	s_add_i32 s15, s25, -1
	s_movk_i32 s7, 0x154
	v_add3_u32 v31, s15, v2, v5
	v_cmp_gt_u32_e32 vcc, s7, v2
	v_cmp_gt_u32_e64 s[4:5], 64, v30
	s_bfe_u32 s27, s2, 0x10004
	s_and_b64 s[4:5], vcc, s[4:5]
	v_cmp_gt_u32_e32 vcc, 64, v31
	v_and_b32_e32 v112, 63, v0
	s_lshl_b32 s39, s27, 7
	s_and_b64 vcc, s[4:5], vcc
	s_waitcnt lgkmcnt(0)
	v_mov_b64_e32 v[6:7], s[16:17]
	v_lshlrev_b32_e32 v2, 1, v4
	s_and_saveexec_b64 s[4:5], vcc
	v_or_b32_e32 v3, s39, v30
	s_lshl_b32 s8, s26, 14
	v_lshlrev_b32_e32 v3, 6, v3
	v_or3_b32 v6, v3, s8, v31
	v_ashrrev_i32_e32 v7, 31, v6
	v_lshlrev_b64 v[6:7], 7, v[6:7]
	v_lshl_add_u64 v[6:7], s[18:19], 0, v[6:7]
	v_mov_b32_e32 v3, 0
	v_lshl_add_u64 v[6:7], v[6:7], 0, v[2:3]
	s_or_b64 exec, exec, s[4:5]
	s_lshl_b32 s37, s3, 10
	v_lshlrev_b32_e32 v5, 4, v112
	v_or_b32_e32 v3, s37, v5
	s_add_i32 s9, s3, 8
	v_readfirstlane_b32 s4, v3
	s_mov_b32 m0, s4
	v_lshl_or_b32 v3, s9, 3, v8
	global_load_lds_dwordx4 v[6:7], off
	s_mov_b32 s8, 0x3c3c3c3d
	v_mul_hi_u32 v6, v3, s8
	v_lshrrev_b32_e32 v6, 3, v6
	v_mul_lo_u32 v7, v6, s6
	v_add_u32_e32 v32, s14, v6
	v_add3_u32 v33, s15, v3, v7
	v_cmp_gt_u32_e64 s[4:5], s7, v3
	v_cmp_gt_u32_e64 s[6:7], 64, v32
	s_and_b64 s[6:7], s[4:5], s[6:7]
	v_cmp_gt_u32_e64 s[4:5], 64, v33
	s_and_b64 s[12:13], s[6:7], s[4:5]
	v_mov_b64_e32 v[6:7], s[16:17]
	s_and_saveexec_b64 s[4:5], s[12:13]
	v_or_b32_e32 v3, s39, v32
	s_lshl_b32 s6, s26, 14
	v_lshlrev_b32_e32 v3, 6, v3
	v_or3_b32 v6, v3, s6, v33
	v_ashrrev_i32_e32 v7, 31, v6
	v_lshlrev_b64 v[6:7], 7, v[6:7]
	v_lshl_add_u64 v[6:7], s[18:19], 0, v[6:7]
	v_mov_b32_e32 v3, 0
	v_lshl_add_u64 v[6:7], v[6:7], 0, v[2:3]
	s_or_b64 exec, exec, s[4:5]
	s_lshl_b32 s38, s9, 10
	v_or_b32_e32 v3, s38, v5
	s_add_i32 s10, s3, 16
	v_readfirstlane_b32 s4, v3
	s_mov_b32 m0, s4
	v_lshl_or_b32 v3, s10, 3, v8
	global_load_lds_dwordx4 v[6:7], off
	v_mul_hi_u32 v6, v3, s8
	v_lshrrev_b32_e32 v6, 3, v6
	s_movk_i32 s8, 0xffde
	v_mul_lo_u32 v7, v6, s8
	v_add_u32_e32 v42, s14, v6
	s_movk_i32 s9, 0x154
	v_add3_u32 v43, s15, v3, v7
	v_cmp_gt_u32_e64 s[4:5], s9, v3
	v_cmp_gt_u32_e64 s[6:7], 64, v42
	s_and_b64 s[6:7], s[4:5], s[6:7]
	v_cmp_gt_u32_e64 s[4:5], 64, v43
	s_and_b64 s[4:5], s[6:7], s[4:5]
	v_mov_b64_e32 v[6:7], s[16:17]
	s_and_saveexec_b64 s[6:7], s[4:5]
	v_or_b32_e32 v3, s39, v42
	s_lshl_b32 s11, s26, 14
	v_lshlrev_b32_e32 v3, 6, v3
	v_or3_b32 v6, v3, s11, v43
	v_ashrrev_i32_e32 v7, 31, v6
	v_lshlrev_b64 v[6:7], 7, v[6:7]
	v_lshl_add_u64 v[6:7], s[18:19], 0, v[6:7]
	v_mov_b32_e32 v3, 0
	v_lshl_add_u64 v[6:7], v[6:7], 0, v[2:3]
	s_or_b64 exec, exec, s[6:7]
	s_lshl_b32 s40, s10, 10
	v_or_b32_e32 v3, s40, v5
	s_add_i32 s11, s3, 24
	v_readfirstlane_b32 s6, v3
	s_mov_b32 m0, s6
	v_lshl_or_b32 v3, s11, 3, v8
	global_load_lds_dwordx4 v[6:7], off
	s_mov_b32 s10, 0x3c3c3c3d
	v_mul_hi_u32 v6, v3, s10
	v_lshrrev_b32_e32 v6, 3, v6
	v_mul_lo_u32 v7, v6, s8
	v_add_u32_e32 v44, s14, v6
	v_add3_u32 v45, s15, v3, v7
	v_cmp_gt_u32_e64 s[6:7], s9, v3
	v_cmp_gt_u32_e64 s[8:9], 64, v44
	s_and_b64 s[8:9], s[6:7], s[8:9]
	v_cmp_gt_u32_e64 s[6:7], 64, v45
	s_and_b64 s[6:7], s[8:9], s[6:7]
	v_mov_b64_e32 v[6:7], s[16:17]
	s_and_saveexec_b64 s[8:9], s[6:7]
	v_or_b32_e32 v3, s39, v44
	s_lshl_b32 s20, s26, 14
	v_lshlrev_b32_e32 v3, 6, v3
	v_or3_b32 v6, v3, s20, v45
	v_ashrrev_i32_e32 v7, 31, v6
	v_lshlrev_b64 v[6:7], 7, v[6:7]
	v_lshl_add_u64 v[6:7], s[18:19], 0, v[6:7]
	v_mov_b32_e32 v3, 0
	v_lshl_add_u64 v[6:7], v[6:7], 0, v[2:3]
	s_or_b64 exec, exec, s[8:9]
	s_lshl_b32 s41, s11, 10
	v_or_b32_e32 v3, s41, v5
	s_add_i32 s20, s3, 32
	v_readfirstlane_b32 s8, v3
	s_mov_b32 m0, s8
	v_lshl_or_b32 v3, s20, 3, v8
	global_load_lds_dwordx4 v[6:7], off
	v_mul_hi_u32 v6, v3, s10
	v_lshrrev_b32_e32 v6, 3, v6
	s_movk_i32 s22, 0xffde
	v_mul_lo_u32 v7, v6, s22
	v_add_u32_e32 v46, s14, v6
	s_movk_i32 s23, 0x154
	v_add3_u32 v47, s15, v3, v7
	v_cmp_gt_u32_e64 s[8:9], s23, v3
	v_cmp_gt_u32_e64 s[10:11], 64, v46
	s_and_b64 s[10:11], s[8:9], s[10:11]
	v_cmp_gt_u32_e64 s[8:9], 64, v47
	s_and_b64 s[8:9], s[10:11], s[8:9]
	v_mov_b64_e32 v[6:7], s[16:17]
	s_and_saveexec_b64 s[10:11], s[8:9]
	v_or_b32_e32 v3, s39, v46
	s_lshl_b32 s21, s26, 14
	v_lshlrev_b32_e32 v3, 6, v3
	v_or3_b32 v6, v3, s21, v47
	v_ashrrev_i32_e32 v7, 31, v6
	v_lshlrev_b64 v[6:7], 7, v[6:7]
	v_lshl_add_u64 v[6:7], s[18:19], 0, v[6:7]
	v_mov_b32_e32 v3, 0
	v_lshl_add_u64 v[6:7], v[6:7], 0, v[2:3]
	s_or_b64 exec, exec, s[10:11]
	s_lshl_b32 s42, s20, 10
	v_or_b32_e32 v2, s42, v5
	s_add_i32 s33, s3, 40
	v_readfirstlane_b32 s10, v2
	s_mov_b32 m0, s10
	v_lshl_or_b32 v2, s33, 3, v8
	global_load_lds_dwordx4 v[6:7], off
	s_mov_b32 s10, 0x3c3c3c3d
	v_mul_hi_u32 v3, v2, s10
	v_lshrrev_b32_e32 v3, 3, v3
	s_mov_b64 s[20:21], s[84:85]
	v_mul_lo_u32 v6, v3, s22
	v_add_u32_e32 v48, s14, v3
	v_add3_u32 v49, s15, v2, v6
	v_cmp_gt_u32_e64 s[10:11], s23, v2
	v_cmp_gt_u32_e64 s[14:15], 64, v48
	s_and_b64 s[14:15], s[10:11], s[14:15]
	v_cmp_gt_u32_e64 s[10:11], 64, v49
	s_and_b64 s[10:11], s[14:15], s[10:11]
	s_xor_b64 s[14:15], s[10:11], -1
	s_and_saveexec_b64 s[22:23], s[14:15]
	s_xor_b64 s[14:15], exec, s[22:23]
	s_lshl_b32 s29, s26, 14
	s_or_saveexec_b64 s[22:23], s[14:15]
	s_mov_b64 s[14:15], s[86:87]
	v_mov_b32_e32 v50, s29
	v_mov_b64_e32 v[2:3], s[16:17]
	s_xor_b64 exec, exec, s[22:23]
	s_cbranch_execz .LBB8_14
	v_or_b32_e32 v2, s39, v48
	s_lshl_b32 s29, s26, 14
	v_lshlrev_b32_e32 v2, 6, v2
	v_or3_b32 v2, v2, s29, v49
	v_ashrrev_i32_e32 v3, 31, v2
	v_lshlrev_b64 v[2:3], 7, v[2:3]
	v_lshl_add_u64 v[2:3], s[18:19], 0, v[2:3]
	v_lshlrev_b32_e32 v6, 1, v4
	v_mov_b32_e32 v7, 0
	v_lshl_add_u64 v[2:3], v[2:3], 0, v[6:7]
	v_mov_b32_e32 v50, s29

_Z6conv_kILi128ELi64ELi20ELi64ELi4ELi4ELb0EEvPKDF16_S1_PKfS3_PDF16_S4_S1_fS3_S3_S3_S3_:
	v_readfirstlane_b32 s37, v0
	v_bfe_u32 v10, v0, 3, 3
	v_and_b32_e32 v1, 7, v0
	s_and_b32 s36, s2, 3
	s_ashr_i32 s35, s2, 6
	s_lshl_b32 s3, s2, 3
	s_lshr_b32 s42, s37, 6
	s_and_b32 s33, s2, 56
	v_bitop3_b32 v2, v10, v1, 6 bitop3:0x6c
	s_mul_i32 s2, s36, 5
	v_lshlrev_b32_e32 v4, 3, v2
	s_add_i32 s24, s2, s33
	v_lshl_or_b32 v2, s42, 3, v10
	s_mov_b32 s2, 0x28282829
	s_load_dwordx2 s[28:29], s[0:1], 0x0
	s_load_dwordx2 s[84:85], s[0:1], 0x8
	s_load_dwordx2 s[86:87], s[0:1], 0x28
	s_load_dwordx2 s[4:5], s[0:1], 0x30
	v_mul_hi_u32 v3, v2, s2
	s_and_b32 s34, s3, 32
	v_lshrrev_b32_e32 v3, 3, v3
	s_movk_i32 s8, 0xffcd
	s_add_i32 s24, s24, -9
	v_mul_lo_u32 v5, v3, s8
	v_add_u32_e32 v103, s24, v3
	s_add_i32 s25, s34, -9
	s_movk_i32 s9, 0x264
	v_add3_u32 v5, s25, v2, v5
	v_cmp_gt_u32_e32 vcc, s9, v2
	v_cmp_gt_u32_e64 s[2:3], 64, v103
	s_and_b64 s[2:3], vcc, s[2:3]
	v_cmp_gt_u32_e32 vcc, 64, v5
	v_and_b32_e32 v102, 63, v0
	s_and_b64 s[6:7], s[2:3], vcc
	s_waitcnt lgkmcnt(0)
	v_mov_b64_e32 v[6:7], s[4:5]
	v_lshlrev_b32_e32 v2, 1, v4
	s_and_saveexec_b64 s[2:3], s[6:7]
	s_lshl_b32 s10, s35, 13
	v_lshlrev_b32_e32 v3, 6, v103
	v_or3_b32 v6, v3, s10, v5
	v_ashrrev_i32_e32 v7, 31, v6
	v_lshlrev_b64 v[6:7], 7, v[6:7]
	v_lshl_add_u64 v[6:7], s[28:29], 0, v[6:7]
	v_mov_b32_e32 v3, 0
	v_lshl_add_u64 v[6:7], v[6:7], 0, v[2:3]
	s_or_b64 exec, exec, s[2:3]
	s_lshl_b32 s44, s42, 10
	v_lshlrev_b32_e32 v104, 4, v102
	v_or_b32_e32 v3, s44, v104
	s_add_i32 s11, s42, 8
	v_readfirstlane_b32 s2, v3
	s_mov_b32 m0, s2
	v_lshl_or_b32 v3, s11, 3, v10
	global_load_lds_dwordx4 v[6:7], off
	s_mov_b32 s10, 0x50505051
	v_mul_hi_u32 v6, v3, s10
	v_lshrrev_b32_e32 v6, 4, v6
	v_mul_lo_u32 v7, v6, s8
	v_add_u32_e32 v105, s24, v6
	v_add3_u32 v8, s25, v3, v7
	v_cmp_gt_u32_e32 vcc, s9, v3
	v_cmp_gt_u32_e64 s[2:3], 64, v105
	s_and_b64 s[2:3], vcc, s[2:3]
	v_cmp_gt_u32_e32 vcc, 64, v8
	s_and_b64 s[8:9], s[2:3], vcc
	v_mov_b64_e32 v[6:7], s[4:5]
	s_and_saveexec_b64 s[2:3], s[8:9]
	s_lshl_b32 s12, s35, 13
	v_lshlrev_b32_e32 v3, 6, v105
	v_or3_b32 v6, v3, s12, v8
	v_ashrrev_i32_e32 v7, 31, v6
	v_lshlrev_b64 v[6:7], 7, v[6:7]
	v_lshl_add_u64 v[6:7], s[28:29], 0, v[6:7]
	v_mov_b32_e32 v3, 0
	v_lshl_add_u64 v[6:7], v[6:7], 0, v[2:3]
	s_or_b64 exec, exec, s[2:3]
	s_lshl_b32 s45, s11, 10
	v_or_b32_e32 v3, s45, v104
	s_add_i32 s14, s42, 16
	v_readfirstlane_b32 s2, v3
	s_mov_b32 m0, s2
	v_lshl_or_b32 v3, s14, 3, v10
	global_load_lds_dwordx4 v[6:7], off
	v_mul_hi_u32 v6, v3, s10
	v_lshrrev_b32_e32 v6, 4, v6
	s_movk_i32 s12, 0xffcd
	v_mul_lo_u32 v7, v6, s12
	v_add_u32_e32 v106, s24, v6
	s_movk_i32 s13, 0x264
	v_add3_u32 v9, s25, v3, v7
	v_cmp_gt_u32_e32 vcc, s13, v3
	v_cmp_gt_u32_e64 s[2:3], 64, v106
	s_and_b64 s[2:3], vcc, s[2:3]
	v_cmp_gt_u32_e32 vcc, 64, v9
	s_and_b64 s[10:11], s[2:3], vcc
	v_mov_b64_e32 v[6:7], s[4:5]
	s_and_saveexec_b64 s[2:3], s[10:11]
	s_lshl_b32 s15, s35, 13
	v_lshlrev_b32_e32 v3, 6, v106
	v_or3_b32 v6, v3, s15, v9
	v_ashrrev_i32_e32 v7, 31, v6
	v_lshlrev_b64 v[6:7], 7, v[6:7]
	v_lshl_add_u64 v[6:7], s[28:29], 0, v[6:7]
	v_mov_b32_e32 v3, 0
	v_lshl_add_u64 v[6:7], v[6:7], 0, v[2:3]
	s_or_b64 exec, exec, s[2:3]
	s_lshl_b32 s46, s14, 10
	v_or_b32_e32 v3, s46, v104
	s_add_i32 s15, s42, 24
	v_readfirstlane_b32 s2, v3
	s_mov_b32 m0, s2
	v_lshl_or_b32 v3, s15, 3, v10
	global_load_lds_dwordx4 v[6:7], off
	s_mov_b32 s14, 0x50505051
	v_mul_hi_u32 v6, v3, s14
	v_lshrrev_b32_e32 v6, 4, v6
	v_mul_lo_u32 v7, v6, s12
	v_add_u32_e32 v107, s24, v6
	v_add3_u32 v11, s25, v3, v7
	v_cmp_gt_u32_e32 vcc, s13, v3
	v_cmp_gt_u32_e64 s[2:3], 64, v107
	s_and_b64 s[2:3], vcc, s[2:3]
	v_cmp_gt_u32_e32 vcc, 64, v11
	s_and_b64 s[12:13], s[2:3], vcc
	v_mov_b64_e32 v[6:7], s[4:5]
	s_and_saveexec_b64 s[2:3], s[12:13]
	s_lshl_b32 s16, s35, 13
	v_lshlrev_b32_e32 v3, 6, v107
	v_or3_b32 v6, v3, s16, v11
	v_ashrrev_i32_e32 v7, 31, v6
	v_lshlrev_b64 v[6:7], 7, v[6:7]
	v_lshl_add_u64 v[6:7], s[28:29], 0, v[6:7]
	v_mov_b32_e32 v3, 0
	v_lshl_add_u64 v[6:7], v[6:7], 0, v[2:3]
	s_or_b64 exec, exec, s[2:3]
	s_lshl_b32 s47, s15, 10
	v_or_b32_e32 v3, s47, v104
	s_add_i32 s18, s42, 32
	v_readfirstlane_b32 s2, v3
	s_mov_b32 m0, s2
	v_lshl_or_b32 v3, s18, 3, v10
	global_load_lds_dwordx4 v[6:7], off
	v_mul_hi_u32 v6, v3, s14
	v_lshrrev_b32_e32 v6, 4, v6
	s_movk_i32 s16, 0xffcd
	v_mul_lo_u32 v7, v6, s16
	v_add_u32_e32 v108, s24, v6
	s_movk_i32 s17, 0x264
	v_add3_u32 v12, s25, v3, v7
	v_cmp_gt_u32_e32 vcc, s17, v3
	v_cmp_gt_u32_e64 s[2:3], 64, v108
	s_and_b64 s[2:3], vcc, s[2:3]
	v_cmp_gt_u32_e32 vcc, 64, v12
	s_and_b64 s[14:15], s[2:3], vcc
	v_mov_b64_e32 v[6:7], s[4:5]
	s_and_saveexec_b64 s[2:3], s[14:15]
	s_lshl_b32 s19, s35, 13
	v_lshlrev_b32_e32 v3, 6, v108
	v_or3_b32 v6, v3, s19, v12
	v_ashrrev_i32_e32 v7, 31, v6
	v_lshlrev_b64 v[6:7], 7, v[6:7]
	v_lshl_add_u64 v[6:7], s[28:29], 0, v[6:7]
	v_mov_b32_e32 v3, 0
	v_lshl_add_u64 v[6:7], v[6:7], 0, v[2:3]
	s_or_b64 exec, exec, s[2:3]
	s_lshl_b32 s48, s18, 10
	v_or_b32_e32 v3, s48, v104
	s_add_i32 s19, s42, 40
	v_readfirstlane_b32 s2, v3
	s_mov_b32 m0, s2
	v_lshl_or_b32 v3, s19, 3, v10
	global_load_lds_dwordx4 v[6:7], off
	s_mov_b32 s18, 0x50505051
	v_mul_hi_u32 v6, v3, s18
	v_lshrrev_b32_e32 v6, 4, v6
	v_mul_lo_u32 v7, v6, s16
	v_add_u32_e32 v109, s24, v6
	v_add3_u32 v13, s25, v3, v7
	v_cmp_gt_u32_e32 vcc, s17, v3
	v_cmp_gt_u32_e64 s[2:3], 64, v109
	s_and_b64 s[2:3], vcc, s[2:3]
	v_cmp_gt_u32_e32 vcc, 64, v13
	s_and_b64 s[16:17], s[2:3], vcc
	v_mov_b64_e32 v[6:7], s[4:5]
	s_and_saveexec_b64 s[2:3], s[16:17]
	s_lshl_b32 s20, s35, 13
	v_lshlrev_b32_e32 v3, 6, v109
	v_or3_b32 v6, v3, s20, v13
	v_ashrrev_i32_e32 v7, 31, v6
	v_lshlrev_b64 v[6:7], 7, v[6:7]
	v_lshl_add_u64 v[6:7], s[28:29], 0, v[6:7]
	v_mov_b32_e32 v3, 0
	v_lshl_add_u64 v[6:7], v[6:7], 0, v[2:3]
	s_or_b64 exec, exec, s[2:3]
	s_lshl_b32 s49, s19, 10
	v_or_b32_e32 v3, s49, v104
	s_add_i32 s22, s42, 48
	v_readfirstlane_b32 s2, v3
	s_mov_b32 m0, s2
	v_lshl_or_b32 v3, s22, 3, v10
	global_load_lds_dwordx4 v[6:7], off
	v_mul_hi_u32 v6, v3, s18
	v_lshrrev_b32_e32 v6, 4, v6
	s_movk_i32 s20, 0xffcd
	v_mul_lo_u32 v7, v6, s20
	v_add_u32_e32 v110, s24, v6
	s_movk_i32 s21, 0x264
	v_add3_u32 v14, s25, v3, v7
	v_cmp_gt_u32_e32 vcc, s21, v3
	v_cmp_gt_u32_e64 s[2:3], 64, v110
	s_and_b64 s[2:3], vcc, s[2:3]
	v_cmp_gt_u32_e32 vcc, 64, v14
	s_and_b64 s[18:19], s[2:3], vcc
	v_mov_b64_e32 v[6:7], s[4:5]
	s_and_saveexec_b64 s[2:3], s[18:19]
	s_lshl_b32 s23, s35, 13
	v_lshlrev_b32_e32 v3, 6, v110
	v_or3_b32 v6, v3, s23, v14
	v_ashrrev_i32_e32 v7, 31, v6
	v_lshlrev_b64 v[6:7], 7, v[6:7]
	v_lshl_add_u64 v[6:7], s[28:29], 0, v[6:7]
	v_mov_b32_e32 v3, 0
	v_lshl_add_u64 v[6:7], v[6:7], 0, v[2:3]
	s_or_b64 exec, exec, s[2:3]
	s_lshl_b32 s50, s22, 10
	v_or_b32_e32 v3, s50, v104
	s_add_i32 s23, s42, 56
	v_readfirstlane_b32 s2, v3
	s_mov_b32 m0, s2
	v_lshl_or_b32 v3, s23, 3, v10
	global_load_lds_dwordx4 v[6:7], off
	s_mov_b32 s22, 0x50505051
	v_mul_hi_u32 v6, v3, s22
	v_lshrrev_b32_e32 v6, 4, v6
	v_mul_lo_u32 v7, v6, s20
	v_add_u32_e32 v113, s24, v6
	v_add3_u32 v15, s25, v3, v7
	v_cmp_gt_u32_e32 vcc, s21, v3
	v_cmp_gt_u32_e64 s[2:3], 64, v113
	s_and_b64 s[2:3], vcc, s[2:3]
	v_cmp_gt_u32_e32 vcc, 64, v15
	s_and_b64 s[20:21], s[2:3], vcc
	v_mov_b64_e32 v[6:7], s[4:5]
	s_and_saveexec_b64 s[2:3], s[20:21]
	s_lshl_b32 s26, s35, 13
	v_lshlrev_b32_e32 v3, 6, v113
	v_or3_b32 v6, v3, s26, v15
	v_ashrrev_i32_e32 v7, 31, v6
	v_lshlrev_b64 v[6:7], 7, v[6:7]
	v_lshl_add_u64 v[6:7], s[28:29], 0, v[6:7]
	v_mov_b32_e32 v3, 0
	v_lshl_add_u64 v[6:7], v[6:7], 0, v[2:3]
	s_or_b64 exec, exec, s[2:3]
	s_lshl_b32 s51, s23, 10
	v_or_b32_e32 v3, s51, v104
	s_add_i32 s26, s42, 64
	v_readfirstlane_b32 s2, v3
	s_mov_b32 m0, s2
	v_lshl_or_b32 v3, s26, 3, v10
	global_load_lds_dwordx4 v[6:7], off
	v_mul_hi_u32 v6, v3, s22
	v_lshrrev_b32_e32 v6, 4, v6
	s_movk_i32 s2, 0xffcd
	v_mul_lo_u32 v7, v6, s2
	v_add_u32_e32 v114, s24, v6
	s_movk_i32 s2, 0x264
	v_add3_u32 v16, s25, v3, v7
	v_cmp_gt_u32_e32 vcc, s2, v3
	v_cmp_gt_u32_e64 s[2:3], 64, v114
	s_and_b64 s[2:3], vcc, s[2:3]
	v_cmp_gt_u32_e32 vcc, 64, v16
	s_and_b64 s[22:23], s[2:3], vcc
	s_xor_b64 s[2:3], s[22:23], -1
	s_and_saveexec_b64 s[30:31], s[2:3]
	s_xor_b64 s[2:3], exec, s[30:31]
	s_lshl_b32 s27, s35, 13
	s_or_saveexec_b64 s[2:3], s[2:3]
	v_mov_b32_e32 v17, s27
	v_mov_b64_e32 v[6:7], s[4:5]
	s_xor_b64 exec, exec, s[2:3]
	s_lshl_b32 s27, s35, 13
	v_lshlrev_b32_e32 v3, 6, v114
	v_or3_b32 v6, v3, s27, v16
	v_ashrrev_i32_e32 v7, 31, v6
	v_lshlrev_b64 v[6:7], 7, v[6:7]
	v_lshl_add_u64 v[6:7], s[28:29], 0, v[6:7]
	v_mov_b32_e32 v3, 0
	v_lshl_add_u64 v[6:7], v[6:7], 0, v[2:3]
	v_mov_b32_e32 v17, s27
	s_or_b64 exec, exec, s[2:3]
	s_lshl_b32 s38, s26, 10
	v_or_b32_e32 v2, s38, v104
	s_add_i32 s41, s42, 0x48
	v_readfirstlane_b32 s2, v2
	s_mov_b32 m0, s2
	v_lshl_or_b32 v2, s41, 3, v10
	global_load_lds_dwordx4 v[6:7], off
	s_mov_b32 s2, 0x50505051
	v_mul_hi_u32 v3, v2, s2
	v_lshrrev_b32_e32 v3, 4, v3
	s_movk_i32 s2, 0xffcd
	s_mov_b64 s[30:31], s[84:85]
	v_mul_lo_u32 v6, v3, s2
	v_add_u32_e32 v115, s24, v3
	s_movk_i32 s2, 0x264
	v_add3_u32 v6, s25, v2, v6
	v_cmp_gt_u32_e32 vcc, s2, v2
	v_cmp_gt_u32_e64 s[2:3], 64, v115
	s_and_b64 s[2:3], vcc, s[2:3]
	v_cmp_gt_u32_e32 vcc, 64, v6
	s_and_b64 s[24:25], s[2:3], vcc
	s_xor_b64 s[2:3], s[24:25], -1
	s_and_saveexec_b64 s[26:27], s[2:3]
	s_xor_b64 s[2:3], exec, s[26:27]
	s_or_saveexec_b64 s[26:27], s[2:3]
	s_mov_b64 s[2:3], s[86:87]
	v_mov_b64_e32 v[2:3], s[4:5]
	s_xor_b64 exec, exec, s[26:27]
	v_lshlrev_b32_e32 v2, 6, v115
	v_or3_b32 v2, v2, v17, v6
	v_ashrrev_i32_e32 v3, 31, v2
	v_lshlrev_b64 v[2:3], 7, v[2:3]
	v_lshl_add_u64 v[2:3], s[28:29], 0, v[2:3]
	v_lshlrev_b32_e32 v18, 1, v4
	v_mov_b32_e32 v19, 0
	v_lshl_add_u64 v[2:3], v[2:3], 0, v[18:19]
	s_or_b64 exec, exec, s[26:27]
	v_lshrrev_b32_e32 v112, 4, v102
	v_lshl_or_b32 v7, v10, 6, s44
	v_bitop3_b32 v10, v112, v0, 6 bitop3:0x78
	v_and_b32_e32 v111, 15, v0
	v_lshlrev_b32_e32 v10, 4, v10
	s_lshr_b32 s40, s37, 8
	v_lshl_or_b32 v10, v111, 7, v10
	v_lshl_or_b32 v10, s40, 13, v10
	s_lshl_b32 s41, s41, 10
	s_movk_i32 s26, 0xdc0
	v_add_u32_e32 v118, 0x14000, v10
	v_or_b32_e32 v10, s41, v104
	v_and_or_b32 v7, v7, s26, v4
	v_readfirstlane_b32 s26, v10
	s_mov_b32 m0, s26
	s_lshl_b32 s55, s42, 11
	s_mul_hi_u32 s26, s37, 0x51eb851f
	s_and_b32 s39, s42, 3
	s_add_i32 s42, s55, 0x14000
	s_lshr_b32 s27, s26, 13
	s_lshr_b32 s52, s26, 14
	s_bitcmp1_b32 s26, 13
	s_cselect_b32 s26, 0x190, 0
	s_sub_i32 s27, s36, s27
	s_add_i32 s27, s27, s52
	s_mulk_i32 s27, 0x64
	s_add_i32 s26, s26, s40
	s_add_i32 s26, s26, s27
	s_ashr_i32 s27, s26, 31
	s_lshl_b64 s[26:27], s[26:27], 13
	s_waitcnt lgkmcnt(0)
	s_add_u32 s26, s30, s26
	s_addc_u32 s27, s31, s27
	s_add_i32 s52, s40, 20
	global_load_lds_dwordx4 v[2:3], off
	v_lshlrev_b32_e32 v2, 1, v7
	s_mov_b32 m0, s42
	s_mul_hi_u32 s53, s52, 0x28f5c29
	global_load_lds_dwordx4 v2, s[26:27]
	s_add_i32 m0, s55, 0x14400
	s_lshr_b32 s56, s53, 1
	s_bitcmp1_b32 s53, 0
	s_cselect_b32 s57, 0x190, 0
	s_sub_i32 s53, s36, s53
	s_add_i32 s53, s53, s56
	s_mulk_i32 s53, 0x64
	s_add_i32 s52, s57, s52
	s_add_i32 s52, s52, s53
	v_mov_b32_e32 v3, 0
	s_ashr_i32 s53, s52, 31
	v_lshl_add_u64 v[18:19], s[26:27], 0, v[2:3]
	s_mov_b64 s[26:27], 0x400
	s_lshl_b64 s[52:53], s[52:53], 13
	v_lshl_add_u64 v[18:19], v[18:19], 0, s[26:27]
	s_add_u32 s52, s30, s52
	global_load_lds_dwordx4 v[18:19], off
	s_addc_u32 s53, s31, s53
	s_add_i32 m0, s55, 0x18000
	v_lshl_add_u64 v[18:19], s[52:53], 0, v[2:3]
	global_load_lds_dwordx4 v2, s[52:53]
	s_add_i32 s52, s40, 40
	s_mul_hi_u32 s53, s52, 0x28f5c29
	s_add_i32 m0, s55, 0x18400
	s_lshr_b32 s56, s53, 1
	s_bitcmp1_b32 s53, 0
	s_cselect_b32 s57, 0x190, 0
	s_sub_i32 s53, s36, s53
	s_add_i32 s53, s53, s56
	s_mulk_i32 s53, 0x64
	s_add_i32 s52, s57, s52
	s_add_i32 s52, s52, s53
	s_ashr_i32 s53, s52, 31
	s_lshl_b64 s[52:53], s[52:53], 13
	s_add_u32 s52, s30, s52
	v_lshl_add_u64 v[18:19], v[18:19], 0, s[26:27]
	s_addc_u32 s53, s31, s53
	global_load_lds_dwordx4 v[18:19], off
	s_add_i32 m0, s55, 0x1c000
	v_lshl_add_u64 v[18:19], s[52:53], 0, v[2:3]
	global_load_lds_dwordx4 v2, s[52:53]
	v_lshl_add_u64 v[18:19], v[18:19], 0, s[26:27]
	s_add_i32 m0, s55, 0x1c400
	s_mul_hi_u32 s52, s40, 0x28f5c29
	global_load_lds_dwordx4 v[18:19], off
	s_mulk_i32 s52, 0x64
	s_sub_i32 s52, s40, s52
	s_mul_i32 s53, s52, 0x67
	s_bfe_u32 s53, s53, 0x5000b
	s_mul_i32 s53, s53, 31
	s_mul_i32 s54, s39, 0x66
	s_and_b32 s53, s53, 0xff
	v_add_u32_e32 v116, s54, v111
	s_add_i32 s52, s52, s53
	s_waitcnt vmcnt(4) lgkmcnt(0)
	s_barrier
	ds_read_b128 v[66:69], v118
	v_add_u32_e32 v7, s52, v116
	v_add_u32_e32 v117, 51, v116
	ds_read_b128 v[70:73], v118 offset:2048
	v_lshlrev_b32_e32 v10, 7, v7
	v_bitop3_b32 v7, v7, v112, 6 bitop3:0x6c
	v_lshl_or_b32 v139, v7, 4, v10
	ds_read_b128 v[74:77], v139
	v_add_u32_e32 v7, s52, v117
	ds_read_b128 v[78:81], v139 offset:2048
	v_lshlrev_b32_e32 v10, 7, v7
	v_bitop3_b32 v7, v7, v112, 6 bitop3:0x6c
	v_lshl_or_b32 v140, v7, 4, v10
	ds_read_b128 v[86:89], v140
	ds_read_b128 v[82:85], v140 offset:2048
	ds_read_b128 v[94:97], v118 offset:4096
	ds_read_b128 v[90:93], v118 offset:6144
	v_add_u32_e32 v120, v17, v5
	v_lshlrev_b32_e32 v4, 1, v4
	v_mov_b32_e32 v5, v3
	v_lshl_add_u64 v[98:99], s[28:29], 0, v[4:5]
	s_add_i32 s28, s40, s54
	v_xor_b32_e32 v119, 64, v118
	s_mov_b32 s43, 0
	v_add_u32_e32 v121, v17, v8
	v_add_u32_e32 v122, v17, v9
	v_add_u32_e32 v123, v17, v11
	v_add_u32_e32 v124, v17, v12
	v_add_u32_e32 v125, v17, v13
	v_add_u32_e32 v126, v17, v14
	v_add_u32_e32 v127, v17, v15
	v_add_u32_e32 v128, v17, v16
	v_add_u32_e32 v129, v17, v6
	v_lshl_add_u64 v[100:101], s[30:31], 0, v[2:3]
	v_add_u32_e32 v130, s28, v111
	v_add_u32_e32 v131, s44, v104
	v_add_u32_e32 v132, s45, v104
	v_add_u32_e32 v133, s46, v104
	v_add_u32_e32 v134, s47, v104
	v_add_u32_e32 v135, s48, v104
	v_add_u32_e32 v136, s49, v104
	v_add_u32_e32 v137, s50, v104
	v_add_u32_e32 v138, s51, v104
	s_mov_b32 s30, s40
	s_mov_b32 s31, s40
	s_mov_b32 s44, 0
	s_mov_b32 s45, 0
	v_mov_b32_e32 v2, v3
	v_mov_b32_e32 v4, v3
	v_mov_b32_e32 v6, v3
	v_mov_b32_e32 v7, v3
	v_mov_b32_e32 v8, v3
	v_mov_b32_e32 v9, v3
	v_mov_b32_e32 v14, v3
	v_mov_b32_e32 v15, v3
	v_mov_b32_e32 v16, v3
	v_mov_b32_e32 v17, v3
	v_mov_b32_e32 v30, v3
	v_mov_b32_e32 v31, v3
	v_mov_b32_e32 v32, v3
	v_mov_b32_e32 v33, v3
	v_mov_b32_e32 v34, v3
	v_mov_b32_e32 v35, v3
	v_mov_b32_e32 v36, v3
	v_mov_b32_e32 v37, v3
	v_mov_b32_e32 v38, v3
	v_mov_b32_e32 v39, v3
	v_mov_b32_e32 v40, v3
	v_mov_b32_e32 v41, v3
	v_mov_b32_e32 v42, v3
	v_mov_b32_e32 v43, v3
	v_mov_b32_e32 v44, v3
	v_mov_b32_e32 v45, v3
	v_mov_b32_e32 v46, v3
	v_mov_b32_e32 v47, v3
	v_mov_b32_e32 v48, v3
	v_mov_b32_e32 v49, v3
	v_mov_b32_e32 v50, v3
	v_mov_b32_e32 v51, v3
	v_mov_b32_e32 v52, v3
	v_mov_b32_e32 v53, v3
	v_mov_b32_e32 v54, v3
	v_mov_b32_e32 v55, v3
	v_mov_b32_e32 v56, v3
	v_mov_b32_e32 v57, v3
	v_mov_b32_e32 v58, v3
	v_mov_b32_e32 v59, v3
	v_mov_b32_e32 v60, v3
	v_mov_b32_e32 v61, v3
	v_mov_b32_e32 v62, v3
	v_mov_b32_e32 v63, v3
	v_mov_b32_e32 v64, v3
	v_mov_b32_e32 v65, v3
	v_mov_b32_e32 v26, v3
	v_mov_b32_e32 v27, v3
	v_mov_b32_e32 v28, v3
	v_mov_b32_e32 v29, v3
	v_mov_b32_e32 v18, v3
	v_mov_b32_e32 v19, v3
	v_mov_b32_e32 v20, v3
	v_mov_b32_e32 v21, v3
	v_mov_b32_e32 v22, v3
	v_mov_b32_e32 v23, v3
	v_mov_b32_e32 v24, v3
	v_mov_b32_e32 v25, v3
	v_mov_b32_e32 v10, v3
	v_mov_b32_e32 v11, v3
	v_mov_b32_e32 v12, v3
	v_mov_b32_e32 v13, v3
	s_mov_b32 s60, 0
	s_mov_b32 s61, 5
	s_mov_b32 s62, 0
	s_mov_b32 s65, 0
	s_mov_b32 s66, 0
	s_mul_i32 s73, s36, 0x64
	s_add_i32 s73, s73, s40
	s_mov_b32 s68, s73
	s_mov_b32 s74, s40
	v_mov_b32_e32 v183, v119
	s_waitcnt lgkmcnt(0)
